# baseline (speedup 1.0000x reference)
.LBB7_3:
	v_add_u32_e32 v67, v80, v77
	s_waitcnt vmcnt(8)
	s_barrier
	s_ashr_i32 s44, s23, 31
	s_xor_b32 s44, s44, s25
	s_abs_i32 s45, s23
	s_mul_hi_u32 s48, s45, s26
	s_mul_i32 s49, s48, s24
	s_sub_i32 s45, s45, s49
	s_add_i32 s49, s48, 1
	s_sub_i32 s46, s45, s24
	s_cmp_ge_u32 s45, s24
	s_cselect_b32 s48, s49, s48
	s_cselect_b32 s45, s46, s45
	s_add_i32 s49, s48, 1
	s_cmp_ge_u32 s45, s24
	s_cselect_b32 s45, s49, s48
	s_xor_b32 s45, s45, s44
	s_sub_i32 s44, s45, s44
	s_mul_i32 s45, s44, s21
	s_sub_i32 s47, s23, s45
	s_lshl_b32 s48, s47, 7
	s_lshl_b32 s46, s44, 7
	s_ashr_i32 s49, s48, 31
	v_or_b32_e32 v152, s46, v1
	v_lshl_add_u64 v[154:155], s[48:49], 1, v[70:71]
	v_mad_i64_i32 v[156:157], s[50:51], v152, s29, v[154:155]
	v_lshl_add_u64 v[158:159], s[48:49], 2, v[68:69]
	v_or_b32_e32 v153, 32, v152
	global_load_dwordx4 v[160:163], v[156:157], off
	v_mad_i64_i32 v[184:185], s[50:51], v153, s29, v[154:155]
	v_or_b32_e32 v153, 64, v152
	global_load_dwordx4 v[176:179], v[158:159], off
	global_load_dwordx4 v[180:183], v[158:159], off offset:16
	v_mad_i64_i32 v[186:187], s[50:51], v153, s29, v[154:155]
	v_or_b32_e32 v153, 0x60, v152
	global_load_dwordx4 v[164:167], v[184:185], off
	v_mad_i64_i32 v[188:189], s[50:51], v153, s29, v[154:155]
	global_load_dwordx4 v[168:171], v[186:187], off
	s_nop 0
	global_load_dwordx4 v[172:175], v[188:189], off
	s_waitcnt lgkmcnt(0)
	ds_read_b128 v[2:5], v67 offset:16384
	v_add_u32_e32 v109, v79, v77
	ds_read_b128 v[6:9], v109
	ds_read_b128 v[10:13], v109 offset:4096
	ds_read_b128 v[14:17], v67 offset:20480
	v_add_u32_e32 v126, v80, v76
	ds_read_b128 v[34:37], v126 offset:16384
	v_add_u32_e32 v127, v79, v76
	s_waitcnt lgkmcnt(3)
	v_mfma_f32_32x32x16_f16 v[50:65], v[2:5], v[6:9], 0
	ds_read_b128 v[110:113], v127
	ds_read_b128 v[114:117], v127 offset:4096
	ds_read_b128 v[118:121], v126 offset:20480
	v_readfirstlane_b32 s2, v0
	s_lshl_b32 s19, s27, 15
	s_lshl_b32 s2, s2, 4
	s_add_i32 s1, s19, 0
	s_and_b32 s31, s2, 0xfffffc00
	s_add_i32 s1, s1, s31
	s_waitcnt lgkmcnt(5)
	v_mfma_f32_32x32x16_f16 v[18:33], v[2:5], v[10:13], 0
	s_mov_b32 m0, s1
	s_add_i32 s2, s1, 0x2000
	buffer_load_dwordx4 v72, s[4:7], s0 offen lds
	s_mov_b32 m0, s2
	s_add_i32 s3, s1, 0x4000
	buffer_load_dwordx4 v74, s[4:7], s0 offen lds
	s_mov_b32 s14, s10
	s_waitcnt lgkmcnt(2)
	v_mfma_f32_32x32x16_f16 v[50:65], v[34:37], v[110:113], v[50:65]
	s_mov_b32 s15, s11
	s_mov_b32 m0, s3
	s_add_i32 s18, s1, 0x6000
	buffer_load_dwordx4 v73, s[12:15], s0 offen lds
	s_mov_b32 m0, s18
	s_add_i32 s33, s19, 0x8000
	buffer_load_dwordx4 v75, s[12:15], s0 offen lds
	s_waitcnt lgkmcnt(1)
	v_mfma_f32_32x32x16_f16 v[18:33], v[34:37], v[114:117], v[18:33]
	s_waitcnt vmcnt(14)
	s_barrier
	s_and_b32 s33, s33, 0x18000
	s_add_i32 s33, s33, 0
	s_add_i32 s33, s33, s31
	s_add_i32 s34, s0, 0x80
	s_mov_b32 m0, s33
	v_mfma_f32_32x32x16_f16 v[34:49], v[14:17], v[6:9], 0
	v_add_u32_e32 v128, v81, v77
	v_add_u32_e32 v129, v82, v77
	v_add_u32_e32 v130, v81, v76
	v_add_u32_e32 v131, v82, v76
	s_xor_b32 s19, s19, 0x10000
	v_add_u32_e32 v134, v83, v77
	v_add_u32_e32 v138, v84, v77
	v_mfma_f32_32x32x16_f16 v[2:17], v[14:17], v[10:13], 0
	v_add_u32_e32 v142, v83, v76
	v_add_u32_e32 v146, v84, v76
	s_waitcnt lgkmcnt(0)
	v_mfma_f32_32x32x16_f16 v[34:49], v[118:121], v[110:113], v[34:49]
	v_mfma_f32_32x32x16_f16 v[2:17], v[118:121], v[114:117], v[2:17]
	ds_read_b128 v[110:113], v67 offset:49152
	ds_read_b128 v[114:117], v109 offset:32768
	ds_read_b128 v[118:121], v109 offset:36864
	ds_read_b128 v[122:125], v67 offset:53248
	s_waitcnt lgkmcnt(2)
	v_mfma_f32_32x32x16_f16 v[50:65], v[110:113], v[114:117], v[50:65]
	s_waitcnt lgkmcnt(1)
	v_mfma_f32_32x32x16_f16 v[18:33], v[110:113], v[118:121], v[18:33]
	s_waitcnt lgkmcnt(0)
	v_mfma_f32_32x32x16_f16 v[34:49], v[122:125], v[114:117], v[34:49]
	v_mfma_f32_32x32x16_f16 v[2:17], v[122:125], v[118:121], v[2:17]
	ds_read_b128 v[110:113], v126 offset:49152
	ds_read_b128 v[114:117], v127 offset:32768
	ds_read_b128 v[118:121], v127 offset:36864
	ds_read_b128 v[122:125], v126 offset:53248
	buffer_load_dwordx4 v72, s[4:7], s34 offen lds
	s_add_i32 m0, s33, 0x2000
	s_nop 0
	buffer_load_dwordx4 v74, s[4:7], s34 offen lds
	s_add_i32 m0, s33, 0x4000
	s_nop 0
	buffer_load_dwordx4 v73, s[12:15], s34 offen lds
	s_add_i32 m0, s33, 0x6000
	s_waitcnt lgkmcnt(2)
	v_mfma_f32_32x32x16_f16 v[50:65], v[110:113], v[114:117], v[50:65]
	buffer_load_dwordx4 v75, s[12:15], s34 offen lds
	s_waitcnt vmcnt(14)
	s_barrier
	s_add_i32 s33, s19, 0
	s_add_i32 s33, s33, s31
	s_add_i32 s34, s0, 0x100
	s_mov_b32 m0, s33
	s_waitcnt lgkmcnt(1)
	v_mfma_f32_32x32x16_f16 v[18:33], v[110:113], v[118:121], v[18:33]
	ds_read_b128 v[110:113], v96
	s_add_i32 s19, s19, 0x8000
	s_and_b32 s19, s19, 0x18000
	s_add_i32 s19, s19, 0
	s_add_i32 s19, s19, s31
	s_add_i32 s31, s0, 0x180
	s_waitcnt lgkmcnt(1)
	v_mfma_f32_32x32x16_f16 v[34:49], v[122:125], v[114:117], v[34:49]
	v_mfma_f32_32x32x16_f16 v[2:17], v[122:125], v[118:121], v[2:17]
	ds_read_b128 v[114:117], v128
	ds_read_b128 v[118:121], v128 offset:4096
	ds_read_b128 v[122:125], v129 offset:4096
	s_waitcnt lgkmcnt(2)
	v_mfma_f32_32x32x16_f16 v[50:65], v[110:113], v[114:117], v[50:65]
	s_waitcnt lgkmcnt(1)
	v_mfma_f32_32x32x16_f16 v[18:33], v[110:113], v[118:121], v[18:33]
	ds_read_b128 v[110:113], v97
	s_waitcnt lgkmcnt(1)
	v_mfma_f32_32x32x16_f16 v[34:49], v[122:125], v[114:117], v[34:49]
	v_mfma_f32_32x32x16_f16 v[2:17], v[122:125], v[118:121], v[2:17]
	ds_read_b128 v[114:117], v130
	ds_read_b128 v[118:121], v130 offset:4096
	ds_read_b128 v[122:125], v131 offset:4096
	buffer_load_dwordx4 v72, s[4:7], s34 offen lds
	s_add_i32 m0, s33, 0x2000
	s_nop 0
	buffer_load_dwordx4 v74, s[4:7], s34 offen lds
	s_add_i32 m0, s33, 0x4000
	s_waitcnt lgkmcnt(2)
	v_mfma_f32_32x32x16_f16 v[50:65], v[110:113], v[114:117], v[50:65]
	buffer_load_dwordx4 v73, s[12:15], s34 offen lds
	s_add_i32 m0, s33, 0x6000
	s_nop 0
	buffer_load_dwordx4 v75, s[12:15], s34 offen lds
	s_waitcnt vmcnt(8)
	s_barrier
	s_mov_b32 m0, s19
	s_waitcnt lgkmcnt(1)
	v_mfma_f32_32x32x16_f16 v[18:33], v[110:113], v[118:121], v[18:33]
	ds_read_b128 v[110:113], v98
	s_waitcnt lgkmcnt(1)
	v_mfma_f32_32x32x16_f16 v[34:49], v[122:125], v[114:117], v[34:49]
	v_mfma_f32_32x32x16_f16 v[2:17], v[122:125], v[118:121], v[2:17]
	ds_read_b128 v[114:117], v134
	ds_read_b128 v[118:121], v134 offset:4096
	ds_read_b128 v[122:125], v138 offset:4096
	s_waitcnt lgkmcnt(2)
	v_mfma_f32_32x32x16_f16 v[50:65], v[110:113], v[114:117], v[50:65]
	s_waitcnt lgkmcnt(1)
	v_mfma_f32_32x32x16_f16 v[18:33], v[110:113], v[118:121], v[18:33]
	ds_read_b128 v[110:113], v99
	s_waitcnt lgkmcnt(1)
	v_mfma_f32_32x32x16_f16 v[34:49], v[122:125], v[114:117], v[34:49]
	v_mfma_f32_32x32x16_f16 v[2:17], v[122:125], v[118:121], v[2:17]
	ds_read_b128 v[114:117], v142
	ds_read_b128 v[118:121], v142 offset:4096
	ds_read_b128 v[122:125], v146 offset:4096
	buffer_load_dwordx4 v72, s[4:7], s31 offen lds
	s_add_i32 m0, s19, 0x2000
	s_nop 0
	buffer_load_dwordx4 v74, s[4:7], s31 offen lds
	s_add_i32 m0, s19, 0x4000
	s_waitcnt lgkmcnt(2)
	v_mfma_f32_32x32x16_f16 v[50:65], v[110:113], v[114:117], v[50:65]
	buffer_load_dwordx4 v73, s[12:15], s31 offen lds
	s_add_i32 m0, s19, 0x6000
	s_nop 0
	buffer_load_dwordx4 v75, s[12:15], s31 offen lds
	s_waitcnt vmcnt(8)
	s_barrier
	s_add_i32 s31, s0, 0x200
	s_waitcnt lgkmcnt(1)
	v_mfma_f32_32x32x16_f16 v[18:33], v[110:113], v[118:121], v[18:33]
	s_mov_b32 m0, s1
	s_abs_i32 s1, s23
	s_ashr_i32 s0, s23, 31
	s_xor_b32 s0, s0, s25
	s_waitcnt lgkmcnt(0)
	v_mfma_f32_32x32x16_f16 v[2:17], v[122:125], v[118:121], v[2:17]
	v_mfma_f32_32x32x16_f16 v[34:49], v[122:125], v[114:117], v[34:49]
	ds_read_b128 v[110:113], v67 offset:16384
	ds_read_b128 v[114:117], v109
	ds_read_b128 v[118:121], v109 offset:4096
	ds_read_b128 v[122:125], v67 offset:20480
	s_waitcnt lgkmcnt(2)
	v_mfma_f32_32x32x16_f16 v[50:65], v[110:113], v[114:117], v[50:65]
	s_waitcnt lgkmcnt(1)
	v_mfma_f32_32x32x16_f16 v[18:33], v[110:113], v[118:121], v[18:33]
	s_waitcnt lgkmcnt(0)
	v_mfma_f32_32x32x16_f16 v[2:17], v[122:125], v[118:121], v[2:17]
	v_mfma_f32_32x32x16_f16 v[34:49], v[122:125], v[114:117], v[34:49]
	ds_read_b128 v[110:113], v126 offset:16384
	ds_read_b128 v[114:117], v127
	ds_read_b128 v[118:121], v127 offset:4096
	ds_read_b128 v[122:125], v126 offset:20480
	buffer_load_dwordx4 v72, s[4:7], s31 offen lds
	s_mov_b32 m0, s2
	s_mul_hi_u32 s2, s1, s26
	buffer_load_dwordx4 v74, s[4:7], s31 offen lds
	s_mov_b32 m0, s3
	s_mul_i32 s3, s2, s24
	s_waitcnt lgkmcnt(2)
	v_mfma_f32_32x32x16_f16 v[50:65], v[110:113], v[114:117], v[50:65]
	buffer_load_dwordx4 v73, s[12:15], s31 offen lds
	s_mov_b32 m0, s18
	s_sub_i32 s1, s1, s3
	buffer_load_dwordx4 v75, s[12:15], s31 offen lds
	s_waitcnt vmcnt(8)
	s_barrier
	s_add_i32 s3, s2, 1
	s_waitcnt lgkmcnt(1)
	v_mfma_f32_32x32x16_f16 v[18:33], v[110:113], v[118:121], v[18:33]
	s_sub_i32 s14, s1, s24
	s_cmp_ge_u32 s1, s24
	s_cselect_b32 s2, s3, s2
	s_cselect_b32 s1, s14, s1
	s_add_i32 s3, s2, 1
	s_cmp_ge_u32 s1, s24
	s_cselect_b32 s1, s3, s2
	s_waitcnt lgkmcnt(0)
	v_mfma_f32_32x32x16_f16 v[2:17], v[122:125], v[118:121], v[2:17]
	s_xor_b32 s1, s1, s0
	s_sub_i32 s0, s1, s0
	s_mul_i32 s1, s0, s21
	s_sub_i32 s15, s23, s1
	s_lshl_b32 s2, s15, 7
	s_lshl_b32 s14, s0, 7
	s_ashr_i32 s3, s2, 31
	v_mfma_f32_32x32x16_f16 v[34:49], v[122:125], v[114:117], v[34:49]
	ds_read_b128 v[110:113], v67 offset:49152
	ds_read_b128 v[114:117], v109 offset:32768
	ds_read_b128 v[118:121], v109 offset:36864
	ds_read_b128 v[122:125], v67 offset:53248
	s_waitcnt lgkmcnt(2)
	v_mfma_f32_32x32x16_f16 v[50:65], v[110:113], v[114:117], v[50:65]
	s_waitcnt lgkmcnt(1)
	v_mfma_f32_32x32x16_f16 v[18:33], v[110:113], v[118:121], v[18:33]
	s_waitcnt lgkmcnt(0)
	v_mfma_f32_32x32x16_f16 v[2:17], v[122:125], v[118:121], v[2:17]
	v_mfma_f32_32x32x16_f16 v[34:49], v[122:125], v[114:117], v[34:49]
	ds_read_b128 v[110:113], v126 offset:49152
	ds_read_b128 v[114:117], v127 offset:32768
	ds_read_b128 v[118:121], v127 offset:36864
	ds_read_b128 v[122:125], v126 offset:53248
	s_waitcnt vmcnt(4)
	s_barrier
	s_waitcnt lgkmcnt(2)
	v_mfma_f32_32x32x16_f16 v[50:65], v[110:113], v[114:117], v[50:65]
	s_waitcnt lgkmcnt(1)
	v_mfma_f32_32x32x16_f16 v[18:33], v[110:113], v[118:121], v[18:33]
	s_waitcnt lgkmcnt(0)
	v_mfma_f32_32x32x16_f16 v[2:17], v[122:125], v[118:121], v[2:17]
	v_mfma_f32_32x32x16_f16 v[34:49], v[122:125], v[114:117], v[34:49]
	ds_read_b128 v[110:113], v96
	ds_read_b128 v[114:117], v128
	ds_read_b128 v[118:121], v128 offset:4096
	ds_read_b128 v[122:125], v129 offset:4096
	s_waitcnt lgkmcnt(2)
	v_mfma_f32_32x32x16_f16 v[50:65], v[110:113], v[114:117], v[50:65]
	s_waitcnt lgkmcnt(1)
	v_mfma_f32_32x32x16_f16 v[18:33], v[110:113], v[118:121], v[18:33]
	s_waitcnt lgkmcnt(0)
	v_mfma_f32_32x32x16_f16 v[2:17], v[122:125], v[118:121], v[2:17]
	v_mfma_f32_32x32x16_f16 v[34:49], v[122:125], v[114:117], v[34:49]
	ds_read_b128 v[110:113], v97
	ds_read_b128 v[114:117], v130
	ds_read_b128 v[126:129], v130 offset:4096
	ds_read_b128 v[130:133], v131 offset:4096
	s_waitcnt vmcnt(0)
	s_barrier
	s_waitcnt lgkmcnt(2)
	v_mfma_f32_32x32x16_f16 v[50:65], v[110:113], v[114:117], v[50:65]
	s_waitcnt lgkmcnt(1)
	v_mfma_f32_32x32x16_f16 v[18:33], v[110:113], v[126:129], v[18:33]
	s_waitcnt lgkmcnt(0)
	v_mfma_f32_32x32x16_f16 v[2:17], v[130:133], v[126:129], v[2:17]
	v_mfma_f32_32x32x16_f16 v[34:49], v[130:133], v[114:117], v[34:49]
	ds_read_b128 v[110:113], v98
	ds_read_b128 v[114:117], v134
	ds_read_b128 v[134:137], v134 offset:4096
	ds_read_b128 v[138:141], v138 offset:4096
	s_waitcnt lgkmcnt(2)
	v_mfma_f32_32x32x16_f16 v[50:65], v[110:113], v[114:117], v[50:65]
	s_waitcnt lgkmcnt(1)
	v_mfma_f32_32x32x16_f16 v[18:33], v[110:113], v[134:137], v[18:33]
	s_waitcnt lgkmcnt(0)
	v_mfma_f32_32x32x16_f16 v[2:17], v[138:141], v[134:137], v[2:17]
	v_mfma_f32_32x32x16_f16 v[34:49], v[138:141], v[114:117], v[34:49]
	ds_read_b128 v[110:113], v99
	ds_read_b128 v[114:117], v142
	ds_read_b128 v[142:145], v142 offset:4096
	ds_read_b128 v[146:149], v146 offset:4096
	s_waitcnt lgkmcnt(0)
	s_barrier
	s_waitcnt lgkmcnt(2)
	v_mfma_f32_32x32x16_f16 v[50:65], v[110:113], v[114:117], v[50:65]
	s_nop 11
	ds_write_b128 v100, v[50:53]
	ds_write_b128 v101, v[54:57]
	s_waitcnt lgkmcnt(3)
	v_mfma_f32_32x32x16_f16 v[18:33], v[110:113], v[142:145], v[18:33]
	s_waitcnt lgkmcnt(2)
	v_mfma_f32_32x32x16_f16 v[2:17], v[146:149], v[142:145], v[2:17]
	v_mfma_f32_32x32x16_f16 v[34:49], v[146:149], v[114:117], v[34:49]
	ds_write_b128 v102, v[58:61]
	ds_write_b128 v103, v[62:65]
	s_nop 9
	ds_write_b128 v104, v[34:37]
	ds_write_b128 v105, v[38:41]
	ds_write_b128 v106, v[42:45]
	ds_write_b128 v107, v[46:49]
	ds_write_b128 v100, v[18:21] offset:16384
	ds_write_b128 v101, v[22:25] offset:16384
	ds_write_b128 v102, v[26:29] offset:16384
	ds_write_b128 v103, v[30:33] offset:16384
	ds_write_b128 v104, v[2:5] offset:16384
	ds_write_b128 v105, v[6:9] offset:16384
	ds_write_b128 v106, v[10:13] offset:16384
	ds_write_b128 v107, v[14:17] offset:16384
	v_or_b32_e32 v25, s14, v1
	s_waitcnt lgkmcnt(0)
	s_barrier
	v_mov_b64_e32 v[10:11], v[160:161]
	v_mov_b64_e32 v[12:13], v[162:163]
	v_mov_b64_e32 v[6:7], v[176:177]
	v_mov_b64_e32 v[8:9], v[178:179]
	v_mov_b64_e32 v[2:3], v[180:181]
	v_mov_b64_e32 v[4:5], v[182:183]
	v_add_u32_e32 v14, 0, v85
	v_add_u32_e32 v18, s28, v85
	ds_read_b128 v[14:17], v14
	ds_read_b128 v[26:29], v18
	v_mov_b64_e32 v[18:19], v[164:165]
	v_mov_b64_e32 v[20:21], v[166:167]
	s_waitcnt lgkmcnt(0)
	v_pk_add_f32 v[16:17], v[16:17], v[28:29]
	v_add_f32_e32 v35, v14, v26
	v_mov_b32_e32 v34, v27
	v_cvt_f32_f16_e32 v30, v11
	v_cvt_f32_f16_sdwa v31, v11 dst_sel:DWORD dst_unused:UNUSED_PAD src0_sel:WORD_1
	v_add_u32_e32 v11, 0, v86
	v_pk_add_f32 v[16:17], v[8:9], v[16:17]
	ds_read_b128 v[26:29], v11
	v_add_u32_e32 v11, s28, v86
	v_pk_add_f32 v[36:37], v[16:17], v[30:31]
	ds_read_b128 v[30:33], v11
	v_cvt_f32_f16_e32 v38, v13
	v_cvt_f32_f16_sdwa v39, v13 dst_sel:DWORD dst_unused:UNUSED_PAD src0_sel:WORD_1
	v_mov_b32_e32 v16, v2
	v_mov_b32_e32 v17, v3
	s_waitcnt lgkmcnt(0)
	v_pk_add_f32 v[28:29], v[28:29], v[32:33]
	v_cvt_f32_f16_e32 v32, v10
	v_pk_add_f32 v[28:29], v[4:5], v[28:29]
	v_pk_mov_b32 v[16:17], v[26:27], v[16:17] op_sel:[1,0]
	v_pk_add_f32 v[28:29], v[28:29], v[38:39]
	v_cvt_f32_f16_e32 v38, v12
	v_add_f32_e32 v26, v26, v30
	v_cvt_f32_f16_sdwa v33, v10 dst_sel:DWORD dst_unused:UNUSED_PAD src0_sel:WORD_1
	v_cvt_f32_f16_sdwa v30, v12 dst_sel:DWORD dst_unused:UNUSED_PAD src0_sel:WORD_1
	v_pk_mov_b32 v[14:15], v[14:15], v[6:7] op_sel:[1,0]
	v_mov_b32_e32 v10, v31
	v_mov_b32_e32 v11, v26
	v_pk_add_f32 v[44:45], v[14:15], v[34:35]
	v_mov_b32_e32 v12, v7
	v_mov_b32_e32 v13, v32
	v_pk_add_f32 v[10:11], v[16:17], v[10:11]
	v_pk_add_f32 v[46:47], v[12:13], v[44:45]
	v_mov_b32_e32 v22, v3
	v_mov_b32_e32 v23, v38
	v_pk_add_f32 v[48:49], v[22:23], v[10:11]
	v_mov_b32_e32 v10, v33
	v_mov_b32_e32 v11, v47
	v_pk_add_f32 v[50:51], v[46:47], v[10:11]
	v_mov_b64_e32 v[14:15], v[168:169]
	v_mov_b64_e32 v[16:17], v[170:171]
	v_mov_b64_e32 v[10:11], v[172:173]
	v_mov_b64_e32 v[12:13], v[174:175]
	v_mov_b32_e32 v31, v49
	v_pk_add_f32 v[40:41], v[48:49], v[30:31]
	v_pk_mov_b32 v[30:31], v[34:35], v[44:45] op_sel:[1,0]
	v_mov_b32_e32 v27, v44
	v_mov_b32_e32 v3, v7
	v_pk_add_f32 v[30:31], v[6:7], v[30:31]
	v_mov_b32_e32 v39, v33
	v_pk_add_f32 v[26:27], v[2:3], v[26:27]
	v_pk_add_f32 v[30:31], v[30:31], v[32:33]
	v_pk_add_f32 v[26:27], v[26:27], v[38:39]
	v_pk_mul_f32 v[32:33], v[46:47], v[46:47]
	v_pk_add_f32 v[34:35], v[30:31], v[26:27]
	v_pk_mul_f32 v[26:27], v[30:31], v[26:27]
	v_mov_b32_e32 v51, v33
	v_pk_mul_f32 v[32:33], v[48:49], v[48:49]
	v_mov_b32_e32 v35, v27
	v_pk_mul_f32 v[26:27], v[40:41], v[40:41]
	v_mov_b32_e32 v32, v40
	v_mov_b32_e32 v67, v26
	v_pk_add_f32 v[32:33], v[50:51], v[32:33]
	v_pk_add_f32 v[26:27], v[34:35], v[66:67]
	v_pk_mul_f32 v[30:31], v[36:37], v[36:37]
	v_pk_mul_f32 v[34:35], v[28:29], v[28:29]
	v_pk_add_f32 v[26:27], v[32:33], v[26:27]
	v_mov_b32_e32 v32, v36
	v_mov_b32_e32 v33, v30
	v_mov_b32_e32 v38, v28
	v_mov_b32_e32 v39, v34
	v_pk_add_f32 v[32:33], v[32:33], v[38:39]
	v_mov_b32_e32 v30, v37
	v_mov_b32_e32 v34, v29
	v_pk_add_f32 v[26:27], v[26:27], v[32:33]
	v_pk_add_f32 v[30:31], v[30:31], v[34:35]
	v_pk_add_f32 v[26:27], v[26:27], v[30:31]
	s_nop 1
	v_mov_b32_dpp v32, v26 row_mirror row_mask:0xf bank_mask:0xf
	v_mov_b32_dpp v33, v27 row_mirror row_mask:0xf bank_mask:0xf
	v_cvt_pk_f16_f32 v39, v28, v29
	v_or_b32_e32 v31, s2, v78
	s_waitcnt lgkmcnt(0)
	v_pk_add_f32 v[26:27], v[26:27], v[32:33]
	s_nop 1
	v_mov_b32_dpp v34, v26 row_half_mirror row_mask:0xf bank_mask:0xf
	v_mov_b32_dpp v35, v27 row_half_mirror row_mask:0xf bank_mask:0xf
	v_cvt_pk_f16_f32 v37, v36, v37
	v_cvt_pk_f16_f32 v36, v47, v50
	s_waitcnt lgkmcnt(0)
	v_pk_add_f32 v[26:27], v[26:27], v[34:35]
	s_nop 1
	v_mov_b32_dpp v28, v26 quad_perm:[2,3,0,1] row_mask:0xf bank_mask:0xf
	v_mov_b32_dpp v29, v27 quad_perm:[2,3,0,1] row_mask:0xf bank_mask:0xf
	v_mul_lo_u32 v24, v25, s30
	v_add_lshl_u32 v24, v31, v24, 1
	v_cvt_pk_f16_f32 v38, v49, v40
	buffer_store_dwordx4 v[36:39], v24, s[8:11], 0 offen sc1
	s_waitcnt lgkmcnt(0)
	v_pk_add_f32 v[26:27], v[26:27], v[28:29]
	s_lshl_b32 s2, s15, 4
	v_mov_b32_e32 v24, v7
	s_nop 1
	v_mov_b32_dpp v28, v26 quad_perm:[1,0,3,2] row_mask:0xf bank_mask:0xf
	v_mov_b32_dpp v29, v27 quad_perm:[1,0,3,2] row_mask:0xf bank_mask:0xf
	s_and_saveexec_b64 s[0:1], vcc
	s_cbranch_execz .LBB7_5
	s_waitcnt lgkmcnt(0)
	v_pk_add_f32 v[64:65], v[26:27], v[28:29]
	v_lshl_add_u32 v23, v25, 6, s2
	v_mov_b32_e32 v67, v66
	s_mov_b32 s18, s10
	s_mov_b32 s19, s11
	buffer_store_dwordx4 v[64:67], v23, s[16:19], 0 offen sc1

.LBB9_3:
	v_add_u32_e32 v110, v80, v76
	s_waitcnt vmcnt(8)
	s_barrier
	s_ashr_i32 s44, s23, 31
	s_xor_b32 s44, s44, s25
	s_abs_i32 s45, s23
	s_mul_hi_u32 s48, s45, s26
	s_mul_i32 s49, s48, s24
	s_sub_i32 s45, s45, s49
	s_add_i32 s49, s48, 1
	s_sub_i32 s46, s45, s24
	s_cmp_ge_u32 s45, s24
	s_cselect_b32 s48, s49, s48
	s_cselect_b32 s45, s46, s45
	s_add_i32 s49, s48, 1
	s_cmp_ge_u32 s45, s24
	s_cselect_b32 s45, s49, s48
	s_xor_b32 s45, s45, s44
	s_sub_i32 s44, s45, s44
	s_mul_i32 s45, s44, s21
	s_sub_i32 s47, s23, s45
	s_lshl_b32 s48, s47, 7
	s_lshl_b32 s46, s44, 7
	s_ashr_i32 s49, s48, 31
	v_or_b32_e32 v152, s46, v1
	v_lshl_add_u64 v[154:155], s[48:49], 1, v[70:71]
	v_mad_i64_i32 v[156:157], s[50:51], v152, s29, v[154:155]
	v_lshl_add_u64 v[158:159], s[48:49], 2, v[68:69]
	v_or_b32_e32 v153, 32, v152
	global_load_dwordx4 v[160:163], v[156:157], off
	v_mad_i64_i32 v[184:185], s[50:51], v153, s29, v[154:155]
	v_or_b32_e32 v153, 64, v152
	global_load_dwordx4 v[176:179], v[158:159], off
	global_load_dwordx4 v[180:183], v[158:159], off offset:16
	v_mad_i64_i32 v[186:187], s[50:51], v153, s29, v[154:155]
	v_or_b32_e32 v153, 0x60, v152
	global_load_dwordx4 v[164:167], v[184:185], off
	v_mad_i64_i32 v[188:189], s[50:51], v153, s29, v[154:155]
	global_load_dwordx4 v[168:171], v[186:187], off
	s_nop 0
	global_load_dwordx4 v[172:175], v[188:189], off
	s_waitcnt lgkmcnt(0)
	ds_read_b128 v[2:5], v110 offset:16384
	v_add_u32_e32 v111, v79, v76
	ds_read_b128 v[6:9], v111
	ds_read_b128 v[10:13], v111 offset:4096
	ds_read_b128 v[14:17], v110 offset:20480
	v_add_u32_e32 v67, v80, v77
	ds_read_b128 v[34:37], v67 offset:16384
	v_add_u32_e32 v109, v79, v77
	s_waitcnt lgkmcnt(3)
	v_mfma_f32_32x32x16_f16 v[50:65], v[2:5], v[6:9], 0
	ds_read_b128 v[112:115], v109
	ds_read_b128 v[116:119], v109 offset:4096
	ds_read_b128 v[120:123], v67 offset:20480
	v_readfirstlane_b32 s2, v0
	s_lshl_b32 s35, s27, 15
	s_lshl_b32 s2, s2, 4
	s_add_i32 s1, s35, 0
	s_and_b32 s39, s2, 0xfffffc00
	s_add_i32 s1, s1, s39
	s_waitcnt lgkmcnt(5)
	v_mfma_f32_32x32x16_f16 v[18:33], v[2:5], v[10:13], 0
	s_mov_b32 m0, s1
	s_add_i32 s2, s1, 0x2000
	buffer_load_dwordx4 v72, s[4:7], s0 offen lds
	s_mov_b32 m0, s2
	s_add_i32 s3, s1, 0x4000
	buffer_load_dwordx4 v74, s[4:7], s0 offen lds
	s_mov_b32 s14, s10
	s_waitcnt lgkmcnt(2)
	v_mfma_f32_32x32x16_f16 v[50:65], v[34:37], v[112:115], v[50:65]
	s_mov_b32 s15, s11
	s_mov_b32 m0, s3
	s_add_i32 s18, s1, 0x6000
	buffer_load_dwordx4 v73, s[12:15], s0 offen lds
	s_mov_b32 m0, s18
	s_add_i32 s19, s35, 0x8000
	buffer_load_dwordx4 v75, s[12:15], s0 offen lds
	s_waitcnt lgkmcnt(1)
	v_mfma_f32_32x32x16_f16 v[18:33], v[34:37], v[116:119], v[18:33]
	s_waitcnt vmcnt(14)
	s_barrier
	s_and_b32 s19, s19, 0x18000
	s_add_i32 s19, s19, 0
	s_add_i32 s19, s19, s39
	s_add_i32 s36, s0, 0x80
	s_mov_b32 m0, s19
	v_mfma_f32_32x32x16_f16 v[34:49], v[14:17], v[6:9], 0
	s_add_i32 s31, s19, 0x2000
	s_add_i32 s33, s19, 0x4000
	s_add_i32 s34, s19, 0x6000
	s_xor_b32 s40, s35, 0x10000
	s_add_i32 s35, s40, 0
	s_add_i32 s35, s35, s39
	s_add_i32 s41, s0, 0x100
	v_mfma_f32_32x32x16_f16 v[2:17], v[14:17], v[10:13], 0
	s_add_i32 s37, s35, 0x4000
	s_add_i32 s38, s35, 0x6000
	s_add_i32 s40, s40, 0x8000
	s_and_b32 s40, s40, 0x18000
	s_add_i32 s40, s40, 0
	s_add_i32 s39, s40, s39
	s_add_i32 s43, s0, 0x180
	s_waitcnt lgkmcnt(0)
	v_mfma_f32_32x32x16_f16 v[34:49], v[120:123], v[112:115], v[34:49]
	s_add_i32 s40, s39, 0x2000
	s_add_i32 s42, s39, 0x6000
	v_mfma_f32_32x32x16_f16 v[2:17], v[120:123], v[116:119], v[2:17]
	ds_read_b128 v[112:115], v110 offset:49152
	ds_read_b128 v[116:119], v111 offset:32768
	ds_read_b128 v[120:123], v111 offset:36864
	ds_read_b128 v[124:127], v110 offset:53248
	s_waitcnt lgkmcnt(2)
	v_mfma_f32_32x32x16_f16 v[50:65], v[112:115], v[116:119], v[50:65]
	s_waitcnt lgkmcnt(1)
	v_mfma_f32_32x32x16_f16 v[18:33], v[112:115], v[120:123], v[18:33]
	s_waitcnt lgkmcnt(0)
	v_mfma_f32_32x32x16_f16 v[34:49], v[124:127], v[116:119], v[34:49]
	v_mfma_f32_32x32x16_f16 v[2:17], v[124:127], v[120:123], v[2:17]
	ds_read_b128 v[112:115], v67 offset:49152
	ds_read_b128 v[116:119], v109 offset:32768
	ds_read_b128 v[120:123], v109 offset:36864
	ds_read_b128 v[124:127], v67 offset:53248
	buffer_load_dwordx4 v72, s[4:7], s36 offen lds
	s_mov_b32 m0, s31
	s_nop 0
	buffer_load_dwordx4 v74, s[4:7], s36 offen lds
	s_mov_b32 m0, s33
	s_nop 0
	buffer_load_dwordx4 v73, s[12:15], s36 offen lds
	s_mov_b32 m0, s34
	s_waitcnt lgkmcnt(2)
	v_mfma_f32_32x32x16_f16 v[50:65], v[112:115], v[116:119], v[50:65]
	buffer_load_dwordx4 v75, s[12:15], s36 offen lds
	s_waitcnt vmcnt(14)
	s_barrier
	s_mov_b32 m0, s35
	s_add_i32 s36, s35, 0x2000
	s_waitcnt lgkmcnt(1)
	v_mfma_f32_32x32x16_f16 v[18:33], v[112:115], v[120:123], v[18:33]
	v_add_u32_e32 v113, v81, v76
	v_add_u32_e32 v112, v82, v76
	s_waitcnt lgkmcnt(0)
	v_mfma_f32_32x32x16_f16 v[34:49], v[124:127], v[116:119], v[34:49]
	ds_read_b128 v[114:117], v96
	v_mfma_f32_32x32x16_f16 v[2:17], v[124:127], v[120:123], v[2:17]
	ds_read_b128 v[118:121], v113
	ds_read_b128 v[122:125], v113 offset:4096
	ds_read_b128 v[126:129], v112 offset:4096
	s_waitcnt lgkmcnt(2)
	v_mfma_f32_32x32x16_f16 v[50:65], v[114:117], v[118:121], v[50:65]
	s_waitcnt lgkmcnt(1)
	v_mfma_f32_32x32x16_f16 v[18:33], v[114:117], v[122:125], v[18:33]
	v_add_u32_e32 v115, v81, v77
	v_add_u32_e32 v114, v82, v77
	s_waitcnt lgkmcnt(0)
	v_mfma_f32_32x32x16_f16 v[34:49], v[126:129], v[118:121], v[34:49]
	ds_read_b128 v[116:119], v97
	v_mfma_f32_32x32x16_f16 v[2:17], v[126:129], v[122:125], v[2:17]
	ds_read_b128 v[120:123], v115
	ds_read_b128 v[124:127], v115 offset:4096
	ds_read_b128 v[128:131], v114 offset:4096
	buffer_load_dwordx4 v72, s[4:7], s41 offen lds
	s_mov_b32 m0, s36
	s_nop 0
	buffer_load_dwordx4 v74, s[4:7], s41 offen lds
	s_mov_b32 m0, s37
	s_waitcnt lgkmcnt(2)
	v_mfma_f32_32x32x16_f16 v[50:65], v[116:119], v[120:123], v[50:65]
	buffer_load_dwordx4 v73, s[12:15], s41 offen lds
	s_mov_b32 m0, s38
	s_nop 0
	buffer_load_dwordx4 v75, s[12:15], s41 offen lds
	s_waitcnt vmcnt(8)
	s_barrier
	s_mov_b32 m0, s39
	s_waitcnt lgkmcnt(1)
	v_mfma_f32_32x32x16_f16 v[18:33], v[116:119], v[124:127], v[18:33]
	v_add_u32_e32 v117, v83, v76
	v_add_u32_e32 v116, v84, v76
	s_add_i32 s41, s39, 0x4000
	s_waitcnt lgkmcnt(0)
	v_mfma_f32_32x32x16_f16 v[34:49], v[128:131], v[120:123], v[34:49]
	ds_read_b128 v[118:121], v98
	v_mfma_f32_32x32x16_f16 v[2:17], v[128:131], v[124:127], v[2:17]
	ds_read_b128 v[122:125], v117
	ds_read_b128 v[126:129], v117 offset:4096
	ds_read_b128 v[130:133], v116 offset:4096
	s_waitcnt lgkmcnt(2)
	v_mfma_f32_32x32x16_f16 v[50:65], v[118:121], v[122:125], v[50:65]
	s_waitcnt lgkmcnt(1)
	v_mfma_f32_32x32x16_f16 v[18:33], v[118:121], v[126:129], v[18:33]
	v_add_u32_e32 v119, v83, v77
	v_add_u32_e32 v118, v84, v77
	s_waitcnt lgkmcnt(0)
	v_mfma_f32_32x32x16_f16 v[34:49], v[130:133], v[122:125], v[34:49]
	ds_read_b128 v[120:123], v99
	v_mfma_f32_32x32x16_f16 v[2:17], v[130:133], v[126:129], v[2:17]
	ds_read_b128 v[124:127], v119
	ds_read_b128 v[128:131], v119 offset:4096
	ds_read_b128 v[132:135], v118 offset:4096
	buffer_load_dwordx4 v72, s[4:7], s43 offen lds
	s_mov_b32 m0, s40
	s_nop 0
	buffer_load_dwordx4 v74, s[4:7], s43 offen lds
	s_mov_b32 m0, s41
	s_waitcnt lgkmcnt(2)
	v_mfma_f32_32x32x16_f16 v[50:65], v[120:123], v[124:127], v[50:65]
	buffer_load_dwordx4 v73, s[12:15], s43 offen lds
	s_mov_b32 m0, s42
	s_nop 0
	buffer_load_dwordx4 v75, s[12:15], s43 offen lds
	s_waitcnt vmcnt(8)
	s_barrier
	s_add_i32 s43, s0, 0x200
	s_waitcnt lgkmcnt(1)
	v_mfma_f32_32x32x16_f16 v[18:33], v[120:123], v[128:131], v[18:33]
	s_mov_b32 m0, s1
	s_waitcnt lgkmcnt(0)
	v_mfma_f32_32x32x16_f16 v[34:49], v[132:135], v[124:127], v[34:49]
	v_mfma_f32_32x32x16_f16 v[2:17], v[132:135], v[128:131], v[2:17]
	ds_read_b128 v[120:123], v110 offset:16384
	ds_read_b128 v[124:127], v111
	ds_read_b128 v[128:131], v111 offset:4096
	ds_read_b128 v[132:135], v110 offset:20480
	s_waitcnt lgkmcnt(2)
	v_mfma_f32_32x32x16_f16 v[50:65], v[120:123], v[124:127], v[50:65]
	s_waitcnt lgkmcnt(1)
	v_mfma_f32_32x32x16_f16 v[18:33], v[120:123], v[128:131], v[18:33]
	s_waitcnt lgkmcnt(0)
	v_mfma_f32_32x32x16_f16 v[34:49], v[132:135], v[124:127], v[34:49]
	v_mfma_f32_32x32x16_f16 v[2:17], v[132:135], v[128:131], v[2:17]
	ds_read_b128 v[120:123], v67 offset:16384
	ds_read_b128 v[124:127], v109
	ds_read_b128 v[128:131], v109 offset:4096
	ds_read_b128 v[132:135], v67 offset:20480
	buffer_load_dwordx4 v72, s[4:7], s43 offen lds
	s_mov_b32 m0, s2
	s_nop 0
	buffer_load_dwordx4 v74, s[4:7], s43 offen lds
	s_mov_b32 m0, s3
	s_waitcnt lgkmcnt(2)
	v_mfma_f32_32x32x16_f16 v[50:65], v[120:123], v[124:127], v[50:65]
	buffer_load_dwordx4 v73, s[12:15], s43 offen lds
	s_mov_b32 m0, s18
	s_nop 0
	buffer_load_dwordx4 v75, s[12:15], s43 offen lds
	s_waitcnt vmcnt(8)
	s_barrier
	s_add_i32 s43, s0, 0x280
	s_waitcnt lgkmcnt(1)
	v_mfma_f32_32x32x16_f16 v[18:33], v[120:123], v[128:131], v[18:33]
	s_mov_b32 m0, s19
	s_waitcnt lgkmcnt(0)
	v_mfma_f32_32x32x16_f16 v[34:49], v[132:135], v[124:127], v[34:49]
	v_mfma_f32_32x32x16_f16 v[2:17], v[132:135], v[128:131], v[2:17]
	ds_read_b128 v[120:123], v110 offset:49152
	ds_read_b128 v[124:127], v111 offset:32768
	ds_read_b128 v[128:131], v111 offset:36864
	ds_read_b128 v[132:135], v110 offset:53248
	s_waitcnt lgkmcnt(2)
	v_mfma_f32_32x32x16_f16 v[50:65], v[120:123], v[124:127], v[50:65]
	s_waitcnt lgkmcnt(1)
	v_mfma_f32_32x32x16_f16 v[18:33], v[120:123], v[128:131], v[18:33]
	s_waitcnt lgkmcnt(0)
	v_mfma_f32_32x32x16_f16 v[34:49], v[132:135], v[124:127], v[34:49]
	v_mfma_f32_32x32x16_f16 v[2:17], v[132:135], v[128:131], v[2:17]
	ds_read_b128 v[120:123], v67 offset:49152
	ds_read_b128 v[124:127], v109 offset:32768
	ds_read_b128 v[128:131], v109 offset:36864
	ds_read_b128 v[132:135], v67 offset:53248
	buffer_load_dwordx4 v72, s[4:7], s43 offen lds
	s_mov_b32 m0, s31
	s_nop 0
	buffer_load_dwordx4 v74, s[4:7], s43 offen lds
	s_mov_b32 m0, s33
	s_waitcnt lgkmcnt(2)
	v_mfma_f32_32x32x16_f16 v[50:65], v[120:123], v[124:127], v[50:65]
	buffer_load_dwordx4 v73, s[12:15], s43 offen lds
	s_mov_b32 m0, s34
	s_nop 0
	buffer_load_dwordx4 v75, s[12:15], s43 offen lds
	s_waitcnt vmcnt(8)
	s_barrier
	s_add_i32 s43, s0, 0x300
	s_waitcnt lgkmcnt(1)
	v_mfma_f32_32x32x16_f16 v[18:33], v[120:123], v[128:131], v[18:33]
	s_mov_b32 m0, s35
	s_waitcnt lgkmcnt(0)
	v_mfma_f32_32x32x16_f16 v[34:49], v[132:135], v[124:127], v[34:49]
	v_mfma_f32_32x32x16_f16 v[2:17], v[132:135], v[128:131], v[2:17]
	ds_read_b128 v[120:123], v96
	ds_read_b128 v[124:127], v113
	ds_read_b128 v[128:131], v113 offset:4096
	ds_read_b128 v[132:135], v112 offset:4096
	s_waitcnt lgkmcnt(2)
	v_mfma_f32_32x32x16_f16 v[50:65], v[120:123], v[124:127], v[50:65]
	s_waitcnt lgkmcnt(1)
	v_mfma_f32_32x32x16_f16 v[18:33], v[120:123], v[128:131], v[18:33]
	s_waitcnt lgkmcnt(0)
	v_mfma_f32_32x32x16_f16 v[34:49], v[132:135], v[124:127], v[34:49]
	v_mfma_f32_32x32x16_f16 v[2:17], v[132:135], v[128:131], v[2:17]
	ds_read_b128 v[120:123], v97
	ds_read_b128 v[124:127], v115
	ds_read_b128 v[128:131], v115 offset:4096
	ds_read_b128 v[132:135], v114 offset:4096
	buffer_load_dwordx4 v72, s[4:7], s43 offen lds
	s_mov_b32 m0, s36
	s_nop 0
	buffer_load_dwordx4 v74, s[4:7], s43 offen lds
	s_mov_b32 m0, s37
	s_waitcnt lgkmcnt(2)
	v_mfma_f32_32x32x16_f16 v[50:65], v[120:123], v[124:127], v[50:65]
	buffer_load_dwordx4 v73, s[12:15], s43 offen lds
	s_mov_b32 m0, s38
	s_nop 0
	buffer_load_dwordx4 v75, s[12:15], s43 offen lds
	s_waitcnt vmcnt(8)
	s_barrier
	s_add_i32 s43, s0, 0x380
	s_waitcnt lgkmcnt(1)
	v_mfma_f32_32x32x16_f16 v[18:33], v[120:123], v[128:131], v[18:33]
	s_mov_b32 m0, s39
	s_waitcnt lgkmcnt(0)
	v_mfma_f32_32x32x16_f16 v[34:49], v[132:135], v[124:127], v[34:49]
	v_mfma_f32_32x32x16_f16 v[2:17], v[132:135], v[128:131], v[2:17]
	ds_read_b128 v[120:123], v98
	ds_read_b128 v[124:127], v117
	ds_read_b128 v[128:131], v117 offset:4096
	ds_read_b128 v[132:135], v116 offset:4096
	s_waitcnt lgkmcnt(2)
	v_mfma_f32_32x32x16_f16 v[50:65], v[120:123], v[124:127], v[50:65]
	s_waitcnt lgkmcnt(1)
	v_mfma_f32_32x32x16_f16 v[18:33], v[120:123], v[128:131], v[18:33]
	s_waitcnt lgkmcnt(0)
	v_mfma_f32_32x32x16_f16 v[34:49], v[132:135], v[124:127], v[34:49]
	v_mfma_f32_32x32x16_f16 v[2:17], v[132:135], v[128:131], v[2:17]
	ds_read_b128 v[120:123], v99
	ds_read_b128 v[124:127], v119
	ds_read_b128 v[128:131], v119 offset:4096
	ds_read_b128 v[132:135], v118 offset:4096
	buffer_load_dwordx4 v72, s[4:7], s43 offen lds
	s_mov_b32 m0, s40
	s_nop 0
	buffer_load_dwordx4 v74, s[4:7], s43 offen lds
	s_mov_b32 m0, s41
	s_waitcnt lgkmcnt(2)
	v_mfma_f32_32x32x16_f16 v[50:65], v[120:123], v[124:127], v[50:65]
	buffer_load_dwordx4 v73, s[12:15], s43 offen lds
	s_mov_b32 m0, s42
	s_nop 0
	buffer_load_dwordx4 v75, s[12:15], s43 offen lds
	s_waitcnt vmcnt(8)
	s_barrier
	s_add_i32 s43, s0, 0x400
	s_waitcnt lgkmcnt(1)
	v_mfma_f32_32x32x16_f16 v[18:33], v[120:123], v[128:131], v[18:33]
	s_mov_b32 m0, s1
	s_waitcnt lgkmcnt(0)
	v_mfma_f32_32x32x16_f16 v[34:49], v[132:135], v[124:127], v[34:49]
	v_mfma_f32_32x32x16_f16 v[2:17], v[132:135], v[128:131], v[2:17]
	ds_read_b128 v[120:123], v110 offset:16384
	ds_read_b128 v[124:127], v111
	ds_read_b128 v[128:131], v111 offset:4096
	ds_read_b128 v[132:135], v110 offset:20480
	s_waitcnt lgkmcnt(2)
	v_mfma_f32_32x32x16_f16 v[50:65], v[120:123], v[124:127], v[50:65]
	s_waitcnt lgkmcnt(1)
	v_mfma_f32_32x32x16_f16 v[18:33], v[120:123], v[128:131], v[18:33]
	s_waitcnt lgkmcnt(0)
	v_mfma_f32_32x32x16_f16 v[34:49], v[132:135], v[124:127], v[34:49]
	v_mfma_f32_32x32x16_f16 v[2:17], v[132:135], v[128:131], v[2:17]
	ds_read_b128 v[120:123], v67 offset:16384
	ds_read_b128 v[124:127], v109
	ds_read_b128 v[128:131], v109 offset:4096
	ds_read_b128 v[132:135], v67 offset:20480
	buffer_load_dwordx4 v72, s[4:7], s43 offen lds
	s_mov_b32 m0, s2
	s_nop 0
	buffer_load_dwordx4 v74, s[4:7], s43 offen lds
	s_mov_b32 m0, s3
	s_waitcnt lgkmcnt(2)
	v_mfma_f32_32x32x16_f16 v[50:65], v[120:123], v[124:127], v[50:65]
	buffer_load_dwordx4 v73, s[12:15], s43 offen lds
	s_mov_b32 m0, s18
	s_nop 0
	buffer_load_dwordx4 v75, s[12:15], s43 offen lds
	s_waitcnt vmcnt(8)
	s_barrier
	s_add_i32 s43, s0, 0x480
	s_waitcnt lgkmcnt(1)
	v_mfma_f32_32x32x16_f16 v[18:33], v[120:123], v[128:131], v[18:33]
	s_mov_b32 m0, s19
	s_waitcnt lgkmcnt(0)
	v_mfma_f32_32x32x16_f16 v[34:49], v[132:135], v[124:127], v[34:49]
	v_mfma_f32_32x32x16_f16 v[2:17], v[132:135], v[128:131], v[2:17]
	ds_read_b128 v[120:123], v110 offset:49152
	ds_read_b128 v[124:127], v111 offset:32768
	ds_read_b128 v[128:131], v111 offset:36864
	ds_read_b128 v[132:135], v110 offset:53248
	s_waitcnt lgkmcnt(2)
	v_mfma_f32_32x32x16_f16 v[50:65], v[120:123], v[124:127], v[50:65]
	s_waitcnt lgkmcnt(1)
	v_mfma_f32_32x32x16_f16 v[18:33], v[120:123], v[128:131], v[18:33]
	s_waitcnt lgkmcnt(0)
	v_mfma_f32_32x32x16_f16 v[34:49], v[132:135], v[124:127], v[34:49]
	v_mfma_f32_32x32x16_f16 v[2:17], v[132:135], v[128:131], v[2:17]
	ds_read_b128 v[120:123], v67 offset:49152
	ds_read_b128 v[124:127], v109 offset:32768
	ds_read_b128 v[128:131], v109 offset:36864
	ds_read_b128 v[132:135], v67 offset:53248
	buffer_load_dwordx4 v72, s[4:7], s43 offen lds
	s_mov_b32 m0, s31
	s_nop 0
	buffer_load_dwordx4 v74, s[4:7], s43 offen lds
	s_mov_b32 m0, s33
	s_waitcnt lgkmcnt(2)
	v_mfma_f32_32x32x16_f16 v[50:65], v[120:123], v[124:127], v[50:65]
	buffer_load_dwordx4 v73, s[12:15], s43 offen lds
	s_mov_b32 m0, s34
	s_nop 0
	buffer_load_dwordx4 v75, s[12:15], s43 offen lds
	s_waitcnt vmcnt(8)
	s_barrier
	s_add_i32 s43, s0, 0x500
	s_waitcnt lgkmcnt(1)
	v_mfma_f32_32x32x16_f16 v[18:33], v[120:123], v[128:131], v[18:33]
	s_mov_b32 m0, s35
	s_waitcnt lgkmcnt(0)
	v_mfma_f32_32x32x16_f16 v[34:49], v[132:135], v[124:127], v[34:49]
	v_mfma_f32_32x32x16_f16 v[2:17], v[132:135], v[128:131], v[2:17]
	ds_read_b128 v[120:123], v96
	ds_read_b128 v[124:127], v113
	ds_read_b128 v[128:131], v113 offset:4096
	ds_read_b128 v[132:135], v112 offset:4096
	s_waitcnt lgkmcnt(2)
	v_mfma_f32_32x32x16_f16 v[50:65], v[120:123], v[124:127], v[50:65]
	s_waitcnt lgkmcnt(1)
	v_mfma_f32_32x32x16_f16 v[18:33], v[120:123], v[128:131], v[18:33]
	s_waitcnt lgkmcnt(0)
	v_mfma_f32_32x32x16_f16 v[34:49], v[132:135], v[124:127], v[34:49]
	v_mfma_f32_32x32x16_f16 v[2:17], v[132:135], v[128:131], v[2:17]
	ds_read_b128 v[120:123], v97
	ds_read_b128 v[124:127], v115
	ds_read_b128 v[128:131], v115 offset:4096
	ds_read_b128 v[132:135], v114 offset:4096
	buffer_load_dwordx4 v72, s[4:7], s43 offen lds
	s_mov_b32 m0, s36
	s_nop 0
	buffer_load_dwordx4 v74, s[4:7], s43 offen lds
	s_mov_b32 m0, s37
	s_waitcnt lgkmcnt(2)
	v_mfma_f32_32x32x16_f16 v[50:65], v[120:123], v[124:127], v[50:65]
	buffer_load_dwordx4 v73, s[12:15], s43 offen lds
	s_mov_b32 m0, s38
	s_nop 0
	buffer_load_dwordx4 v75, s[12:15], s43 offen lds
	s_waitcnt vmcnt(8)
	s_barrier
	s_add_i32 s43, s0, 0x580
	s_waitcnt lgkmcnt(1)
	v_mfma_f32_32x32x16_f16 v[18:33], v[120:123], v[128:131], v[18:33]
	s_mov_b32 m0, s39
	s_waitcnt lgkmcnt(0)
	v_mfma_f32_32x32x16_f16 v[34:49], v[132:135], v[124:127], v[34:49]
	v_mfma_f32_32x32x16_f16 v[2:17], v[132:135], v[128:131], v[2:17]
	ds_read_b128 v[120:123], v98
	ds_read_b128 v[124:127], v117
	ds_read_b128 v[128:131], v117 offset:4096
	ds_read_b128 v[132:135], v116 offset:4096
	s_waitcnt lgkmcnt(2)
	v_mfma_f32_32x32x16_f16 v[50:65], v[120:123], v[124:127], v[50:65]
	s_waitcnt lgkmcnt(1)
	v_mfma_f32_32x32x16_f16 v[18:33], v[120:123], v[128:131], v[18:33]
	s_waitcnt lgkmcnt(0)
	v_mfma_f32_32x32x16_f16 v[34:49], v[132:135], v[124:127], v[34:49]
	v_mfma_f32_32x32x16_f16 v[2:17], v[132:135], v[128:131], v[2:17]
	ds_read_b128 v[120:123], v99
	ds_read_b128 v[124:127], v119
	ds_read_b128 v[128:131], v119 offset:4096
	ds_read_b128 v[132:135], v118 offset:4096
	buffer_load_dwordx4 v72, s[4:7], s43 offen lds
	s_mov_b32 m0, s40
	s_nop 0
	buffer_load_dwordx4 v74, s[4:7], s43 offen lds
	s_mov_b32 m0, s41
	s_waitcnt lgkmcnt(2)
	v_mfma_f32_32x32x16_f16 v[50:65], v[120:123], v[124:127], v[50:65]
	buffer_load_dwordx4 v73, s[12:15], s43 offen lds
	s_mov_b32 m0, s42
	s_nop 0
	buffer_load_dwordx4 v75, s[12:15], s43 offen lds
	s_waitcnt vmcnt(8)
	s_barrier
	s_add_i32 s43, s0, 0x600
	s_waitcnt lgkmcnt(1)
	v_mfma_f32_32x32x16_f16 v[18:33], v[120:123], v[128:131], v[18:33]
	s_mov_b32 m0, s1
	s_waitcnt lgkmcnt(0)
	v_mfma_f32_32x32x16_f16 v[34:49], v[132:135], v[124:127], v[34:49]
	v_mfma_f32_32x32x16_f16 v[2:17], v[132:135], v[128:131], v[2:17]
	ds_read_b128 v[120:123], v110 offset:16384
	ds_read_b128 v[124:127], v111
	ds_read_b128 v[128:131], v111 offset:4096
	ds_read_b128 v[132:135], v110 offset:20480
	s_waitcnt lgkmcnt(2)
	v_mfma_f32_32x32x16_f16 v[50:65], v[120:123], v[124:127], v[50:65]
	s_waitcnt lgkmcnt(1)
	v_mfma_f32_32x32x16_f16 v[18:33], v[120:123], v[128:131], v[18:33]
	s_waitcnt lgkmcnt(0)
	v_mfma_f32_32x32x16_f16 v[34:49], v[132:135], v[124:127], v[34:49]
	v_mfma_f32_32x32x16_f16 v[2:17], v[132:135], v[128:131], v[2:17]
	ds_read_b128 v[120:123], v67 offset:16384
	ds_read_b128 v[124:127], v109
	ds_read_b128 v[128:131], v109 offset:4096
	ds_read_b128 v[132:135], v67 offset:20480
	buffer_load_dwordx4 v72, s[4:7], s43 offen lds
	s_mov_b32 m0, s2
	s_nop 0
	buffer_load_dwordx4 v74, s[4:7], s43 offen lds
	s_mov_b32 m0, s3
	s_waitcnt lgkmcnt(2)
	v_mfma_f32_32x32x16_f16 v[50:65], v[120:123], v[124:127], v[50:65]
	buffer_load_dwordx4 v73, s[12:15], s43 offen lds
	s_mov_b32 m0, s18
	s_nop 0
	buffer_load_dwordx4 v75, s[12:15], s43 offen lds
	s_waitcnt vmcnt(8)
	s_barrier
	s_add_i32 s43, s0, 0x680
	s_waitcnt lgkmcnt(1)
	v_mfma_f32_32x32x16_f16 v[18:33], v[120:123], v[128:131], v[18:33]
	s_mov_b32 m0, s19
	s_waitcnt lgkmcnt(0)
	v_mfma_f32_32x32x16_f16 v[34:49], v[132:135], v[124:127], v[34:49]
	v_mfma_f32_32x32x16_f16 v[2:17], v[132:135], v[128:131], v[2:17]
	ds_read_b128 v[120:123], v110 offset:49152
	ds_read_b128 v[124:127], v111 offset:32768
	ds_read_b128 v[128:131], v111 offset:36864
	ds_read_b128 v[132:135], v110 offset:53248
	s_waitcnt lgkmcnt(2)
	v_mfma_f32_32x32x16_f16 v[50:65], v[120:123], v[124:127], v[50:65]
	s_waitcnt lgkmcnt(1)
	v_mfma_f32_32x32x16_f16 v[18:33], v[120:123], v[128:131], v[18:33]
	s_waitcnt lgkmcnt(0)
	v_mfma_f32_32x32x16_f16 v[34:49], v[132:135], v[124:127], v[34:49]
	v_mfma_f32_32x32x16_f16 v[2:17], v[132:135], v[128:131], v[2:17]
	ds_read_b128 v[120:123], v67 offset:49152
	ds_read_b128 v[124:127], v109 offset:32768
	ds_read_b128 v[128:131], v109 offset:36864
	ds_read_b128 v[132:135], v67 offset:53248
	buffer_load_dwordx4 v72, s[4:7], s43 offen lds
	s_mov_b32 m0, s31
	s_nop 0
	buffer_load_dwordx4 v74, s[4:7], s43 offen lds
	s_mov_b32 m0, s33
	s_waitcnt lgkmcnt(2)
	v_mfma_f32_32x32x16_f16 v[50:65], v[120:123], v[124:127], v[50:65]
	buffer_load_dwordx4 v73, s[12:15], s43 offen lds
	s_mov_b32 m0, s34
	s_nop 0
	buffer_load_dwordx4 v75, s[12:15], s43 offen lds
	s_waitcnt vmcnt(8)
	s_barrier
	s_add_i32 s43, s0, 0x700
	s_waitcnt lgkmcnt(1)
	v_mfma_f32_32x32x16_f16 v[18:33], v[120:123], v[128:131], v[18:33]
	s_mov_b32 m0, s35
	s_waitcnt lgkmcnt(0)
	v_mfma_f32_32x32x16_f16 v[34:49], v[132:135], v[124:127], v[34:49]
	v_mfma_f32_32x32x16_f16 v[2:17], v[132:135], v[128:131], v[2:17]
	ds_read_b128 v[120:123], v96
	ds_read_b128 v[124:127], v113
	ds_read_b128 v[128:131], v113 offset:4096
	ds_read_b128 v[132:135], v112 offset:4096
	s_waitcnt lgkmcnt(2)
	v_mfma_f32_32x32x16_f16 v[50:65], v[120:123], v[124:127], v[50:65]
	s_waitcnt lgkmcnt(1)
	v_mfma_f32_32x32x16_f16 v[18:33], v[120:123], v[128:131], v[18:33]
	s_waitcnt lgkmcnt(0)
	v_mfma_f32_32x32x16_f16 v[34:49], v[132:135], v[124:127], v[34:49]
	v_mfma_f32_32x32x16_f16 v[2:17], v[132:135], v[128:131], v[2:17]
	ds_read_b128 v[120:123], v97
	ds_read_b128 v[124:127], v115
	ds_read_b128 v[128:131], v115 offset:4096
	ds_read_b128 v[132:135], v114 offset:4096
	buffer_load_dwordx4 v72, s[4:7], s43 offen lds
	s_mov_b32 m0, s36
	s_nop 0
	buffer_load_dwordx4 v74, s[4:7], s43 offen lds
	s_mov_b32 m0, s37
	s_waitcnt lgkmcnt(2)
	v_mfma_f32_32x32x16_f16 v[50:65], v[120:123], v[124:127], v[50:65]
	buffer_load_dwordx4 v73, s[12:15], s43 offen lds
	s_mov_b32 m0, s38
	s_nop 0
	buffer_load_dwordx4 v75, s[12:15], s43 offen lds
	s_waitcnt vmcnt(8)
	s_barrier
	s_add_i32 s43, s0, 0x780
	s_waitcnt lgkmcnt(1)
	v_mfma_f32_32x32x16_f16 v[18:33], v[120:123], v[128:131], v[18:33]
	s_mov_b32 m0, s39
	s_waitcnt lgkmcnt(0)
	v_mfma_f32_32x32x16_f16 v[34:49], v[132:135], v[124:127], v[34:49]
	v_mfma_f32_32x32x16_f16 v[2:17], v[132:135], v[128:131], v[2:17]
	ds_read_b128 v[120:123], v98
	ds_read_b128 v[124:127], v117
	ds_read_b128 v[128:131], v117 offset:4096
	ds_read_b128 v[132:135], v116 offset:4096
	s_waitcnt lgkmcnt(2)
	v_mfma_f32_32x32x16_f16 v[50:65], v[120:123], v[124:127], v[50:65]
	s_waitcnt lgkmcnt(1)
	v_mfma_f32_32x32x16_f16 v[18:33], v[120:123], v[128:131], v[18:33]
	s_waitcnt lgkmcnt(0)
	v_mfma_f32_32x32x16_f16 v[34:49], v[132:135], v[124:127], v[34:49]
	v_mfma_f32_32x32x16_f16 v[2:17], v[132:135], v[128:131], v[2:17]
	ds_read_b128 v[120:123], v99
	ds_read_b128 v[124:127], v119
	ds_read_b128 v[128:131], v119 offset:4096
	ds_read_b128 v[132:135], v118 offset:4096
	buffer_load_dwordx4 v72, s[4:7], s43 offen lds
	s_mov_b32 m0, s40
	s_nop 0
	buffer_load_dwordx4 v74, s[4:7], s43 offen lds
	s_mov_b32 m0, s41
	s_waitcnt lgkmcnt(2)
	v_mfma_f32_32x32x16_f16 v[50:65], v[120:123], v[124:127], v[50:65]
	buffer_load_dwordx4 v73, s[12:15], s43 offen lds
	s_mov_b32 m0, s42
	s_nop 0
	buffer_load_dwordx4 v75, s[12:15], s43 offen lds
	s_waitcnt vmcnt(8)
	s_barrier
	s_add_i32 s43, s0, 0x800
	s_waitcnt lgkmcnt(1)
	v_mfma_f32_32x32x16_f16 v[18:33], v[120:123], v[128:131], v[18:33]
	s_mov_b32 m0, s1
	s_waitcnt lgkmcnt(0)
	v_mfma_f32_32x32x16_f16 v[34:49], v[132:135], v[124:127], v[34:49]
	v_mfma_f32_32x32x16_f16 v[2:17], v[132:135], v[128:131], v[2:17]
	ds_read_b128 v[120:123], v110 offset:16384
	ds_read_b128 v[124:127], v111
	ds_read_b128 v[128:131], v111 offset:4096
	ds_read_b128 v[132:135], v110 offset:20480
	s_waitcnt lgkmcnt(2)
	v_mfma_f32_32x32x16_f16 v[50:65], v[120:123], v[124:127], v[50:65]
	s_waitcnt lgkmcnt(1)
	v_mfma_f32_32x32x16_f16 v[18:33], v[120:123], v[128:131], v[18:33]
	s_waitcnt lgkmcnt(0)
	v_mfma_f32_32x32x16_f16 v[34:49], v[132:135], v[124:127], v[34:49]
	v_mfma_f32_32x32x16_f16 v[2:17], v[132:135], v[128:131], v[2:17]
	ds_read_b128 v[120:123], v67 offset:16384
	ds_read_b128 v[124:127], v109
	ds_read_b128 v[128:131], v109 offset:4096
	ds_read_b128 v[132:135], v67 offset:20480
	buffer_load_dwordx4 v72, s[4:7], s43 offen lds
	s_mov_b32 m0, s2
	s_nop 0
	buffer_load_dwordx4 v74, s[4:7], s43 offen lds
	s_mov_b32 m0, s3
	s_waitcnt lgkmcnt(2)
	v_mfma_f32_32x32x16_f16 v[50:65], v[120:123], v[124:127], v[50:65]
	buffer_load_dwordx4 v73, s[12:15], s43 offen lds
	s_mov_b32 m0, s18
	s_nop 0
	buffer_load_dwordx4 v75, s[12:15], s43 offen lds
	s_waitcnt vmcnt(8)
	s_barrier
	s_add_i32 s43, s0, 0x880
	s_waitcnt lgkmcnt(1)
	v_mfma_f32_32x32x16_f16 v[18:33], v[120:123], v[128:131], v[18:33]
	s_mov_b32 m0, s19
	s_waitcnt lgkmcnt(0)
	v_mfma_f32_32x32x16_f16 v[34:49], v[132:135], v[124:127], v[34:49]
	v_mfma_f32_32x32x16_f16 v[2:17], v[132:135], v[128:131], v[2:17]
	ds_read_b128 v[120:123], v110 offset:49152
	ds_read_b128 v[124:127], v111 offset:32768
	ds_read_b128 v[128:131], v111 offset:36864
	ds_read_b128 v[132:135], v110 offset:53248
	s_waitcnt lgkmcnt(2)
	v_mfma_f32_32x32x16_f16 v[50:65], v[120:123], v[124:127], v[50:65]
	s_waitcnt lgkmcnt(1)
	v_mfma_f32_32x32x16_f16 v[18:33], v[120:123], v[128:131], v[18:33]
	s_waitcnt lgkmcnt(0)
	v_mfma_f32_32x32x16_f16 v[34:49], v[132:135], v[124:127], v[34:49]
	v_mfma_f32_32x32x16_f16 v[2:17], v[132:135], v[128:131], v[2:17]
	ds_read_b128 v[120:123], v67 offset:49152
	ds_read_b128 v[124:127], v109 offset:32768
	ds_read_b128 v[128:131], v109 offset:36864
	ds_read_b128 v[132:135], v67 offset:53248
	buffer_load_dwordx4 v72, s[4:7], s43 offen lds
	s_mov_b32 m0, s31
	s_nop 0
	buffer_load_dwordx4 v74, s[4:7], s43 offen lds
	s_mov_b32 m0, s33
	s_waitcnt lgkmcnt(2)
	v_mfma_f32_32x32x16_f16 v[50:65], v[120:123], v[124:127], v[50:65]
	buffer_load_dwordx4 v73, s[12:15], s43 offen lds
	s_mov_b32 m0, s34
	s_nop 0
	buffer_load_dwordx4 v75, s[12:15], s43 offen lds
	s_waitcnt vmcnt(8)
	s_barrier
	s_add_i32 s43, s0, 0x900
	s_waitcnt lgkmcnt(1)
	v_mfma_f32_32x32x16_f16 v[18:33], v[120:123], v[128:131], v[18:33]
	s_mov_b32 m0, s35
	s_waitcnt lgkmcnt(0)
	v_mfma_f32_32x32x16_f16 v[34:49], v[132:135], v[124:127], v[34:49]
	v_mfma_f32_32x32x16_f16 v[2:17], v[132:135], v[128:131], v[2:17]
	ds_read_b128 v[120:123], v96
	ds_read_b128 v[124:127], v113
	ds_read_b128 v[128:131], v113 offset:4096
	ds_read_b128 v[132:135], v112 offset:4096
	s_waitcnt lgkmcnt(2)
	v_mfma_f32_32x32x16_f16 v[50:65], v[120:123], v[124:127], v[50:65]
	s_waitcnt lgkmcnt(1)
	v_mfma_f32_32x32x16_f16 v[18:33], v[120:123], v[128:131], v[18:33]
	s_waitcnt lgkmcnt(0)
	v_mfma_f32_32x32x16_f16 v[34:49], v[132:135], v[124:127], v[34:49]
	v_mfma_f32_32x32x16_f16 v[2:17], v[132:135], v[128:131], v[2:17]
	ds_read_b128 v[120:123], v97
	ds_read_b128 v[124:127], v115
	ds_read_b128 v[128:131], v115 offset:4096
	ds_read_b128 v[132:135], v114 offset:4096
	buffer_load_dwordx4 v72, s[4:7], s43 offen lds
	s_mov_b32 m0, s36
	s_nop 0
	buffer_load_dwordx4 v74, s[4:7], s43 offen lds
	s_mov_b32 m0, s37
	s_waitcnt lgkmcnt(2)
	v_mfma_f32_32x32x16_f16 v[50:65], v[120:123], v[124:127], v[50:65]
	buffer_load_dwordx4 v73, s[12:15], s43 offen lds
	s_mov_b32 m0, s38
	s_nop 0
	buffer_load_dwordx4 v75, s[12:15], s43 offen lds
	s_waitcnt vmcnt(8)
	s_barrier
	s_add_i32 s43, s0, 0x980
	s_waitcnt lgkmcnt(1)
	v_mfma_f32_32x32x16_f16 v[18:33], v[120:123], v[128:131], v[18:33]
	s_mov_b32 m0, s39
	s_waitcnt lgkmcnt(0)
	v_mfma_f32_32x32x16_f16 v[34:49], v[132:135], v[124:127], v[34:49]
	v_mfma_f32_32x32x16_f16 v[2:17], v[132:135], v[128:131], v[2:17]
	ds_read_b128 v[120:123], v98
	ds_read_b128 v[124:127], v117
	ds_read_b128 v[128:131], v117 offset:4096
	ds_read_b128 v[132:135], v116 offset:4096
	s_waitcnt lgkmcnt(2)
	v_mfma_f32_32x32x16_f16 v[50:65], v[120:123], v[124:127], v[50:65]
	s_waitcnt lgkmcnt(1)
	v_mfma_f32_32x32x16_f16 v[18:33], v[120:123], v[128:131], v[18:33]
	s_waitcnt lgkmcnt(0)
	v_mfma_f32_32x32x16_f16 v[34:49], v[132:135], v[124:127], v[34:49]
	v_mfma_f32_32x32x16_f16 v[2:17], v[132:135], v[128:131], v[2:17]
	ds_read_b128 v[120:123], v99
	ds_read_b128 v[124:127], v119
	ds_read_b128 v[128:131], v119 offset:4096
	ds_read_b128 v[132:135], v118 offset:4096
	buffer_load_dwordx4 v72, s[4:7], s43 offen lds
	s_mov_b32 m0, s40
	s_nop 0
	buffer_load_dwordx4 v74, s[4:7], s43 offen lds
	s_mov_b32 m0, s41
	s_waitcnt lgkmcnt(2)
	v_mfma_f32_32x32x16_f16 v[50:65], v[120:123], v[124:127], v[50:65]
	buffer_load_dwordx4 v73, s[12:15], s43 offen lds
	s_mov_b32 m0, s42
	s_nop 0
	buffer_load_dwordx4 v75, s[12:15], s43 offen lds
	s_waitcnt vmcnt(8)
	s_barrier
	s_add_i32 s43, s0, 0xa00
	s_waitcnt lgkmcnt(1)
	v_mfma_f32_32x32x16_f16 v[18:33], v[120:123], v[128:131], v[18:33]
	s_mov_b32 m0, s1
	s_waitcnt lgkmcnt(0)
	v_mfma_f32_32x32x16_f16 v[34:49], v[132:135], v[124:127], v[34:49]
	v_mfma_f32_32x32x16_f16 v[2:17], v[132:135], v[128:131], v[2:17]
	ds_read_b128 v[120:123], v110 offset:16384
	ds_read_b128 v[124:127], v111
	ds_read_b128 v[128:131], v111 offset:4096
	ds_read_b128 v[132:135], v110 offset:20480
	s_waitcnt lgkmcnt(2)
	v_mfma_f32_32x32x16_f16 v[50:65], v[120:123], v[124:127], v[50:65]
	s_waitcnt lgkmcnt(1)
	v_mfma_f32_32x32x16_f16 v[18:33], v[120:123], v[128:131], v[18:33]
	s_waitcnt lgkmcnt(0)
	v_mfma_f32_32x32x16_f16 v[34:49], v[132:135], v[124:127], v[34:49]
	v_mfma_f32_32x32x16_f16 v[2:17], v[132:135], v[128:131], v[2:17]
	ds_read_b128 v[120:123], v67 offset:16384
	ds_read_b128 v[124:127], v109
	ds_read_b128 v[128:131], v109 offset:4096
	ds_read_b128 v[132:135], v67 offset:20480
	buffer_load_dwordx4 v72, s[4:7], s43 offen lds
	s_mov_b32 m0, s2
	s_nop 0
	buffer_load_dwordx4 v74, s[4:7], s43 offen lds
	s_mov_b32 m0, s3
	s_waitcnt lgkmcnt(2)
	v_mfma_f32_32x32x16_f16 v[50:65], v[120:123], v[124:127], v[50:65]
	buffer_load_dwordx4 v73, s[12:15], s43 offen lds
	s_mov_b32 m0, s18
	s_nop 0
	buffer_load_dwordx4 v75, s[12:15], s43 offen lds
	s_waitcnt vmcnt(8)
	s_barrier
	s_add_i32 s43, s0, 0xa80
	s_waitcnt lgkmcnt(1)
	v_mfma_f32_32x32x16_f16 v[18:33], v[120:123], v[128:131], v[18:33]
	s_mov_b32 m0, s19
	s_waitcnt lgkmcnt(0)
	v_mfma_f32_32x32x16_f16 v[34:49], v[132:135], v[124:127], v[34:49]
	v_mfma_f32_32x32x16_f16 v[2:17], v[132:135], v[128:131], v[2:17]
	ds_read_b128 v[120:123], v110 offset:49152
	ds_read_b128 v[124:127], v111 offset:32768
	ds_read_b128 v[128:131], v111 offset:36864
	ds_read_b128 v[132:135], v110 offset:53248
	s_waitcnt lgkmcnt(2)
	v_mfma_f32_32x32x16_f16 v[50:65], v[120:123], v[124:127], v[50:65]
	s_waitcnt lgkmcnt(1)
	v_mfma_f32_32x32x16_f16 v[18:33], v[120:123], v[128:131], v[18:33]
	s_waitcnt lgkmcnt(0)
	v_mfma_f32_32x32x16_f16 v[34:49], v[132:135], v[124:127], v[34:49]
	v_mfma_f32_32x32x16_f16 v[2:17], v[132:135], v[128:131], v[2:17]
	ds_read_b128 v[120:123], v67 offset:49152
	ds_read_b128 v[124:127], v109 offset:32768
	ds_read_b128 v[128:131], v109 offset:36864
	ds_read_b128 v[132:135], v67 offset:53248
	buffer_load_dwordx4 v72, s[4:7], s43 offen lds
	s_mov_b32 m0, s31
	s_nop 0
	buffer_load_dwordx4 v74, s[4:7], s43 offen lds
	s_mov_b32 m0, s33
	s_waitcnt lgkmcnt(2)
	v_mfma_f32_32x32x16_f16 v[50:65], v[120:123], v[124:127], v[50:65]
	buffer_load_dwordx4 v73, s[12:15], s43 offen lds
	s_mov_b32 m0, s34
	s_nop 0
	buffer_load_dwordx4 v75, s[12:15], s43 offen lds
	s_waitcnt vmcnt(8)
	s_barrier
	s_add_i32 s43, s0, 0xb00
	s_waitcnt lgkmcnt(1)
	v_mfma_f32_32x32x16_f16 v[18:33], v[120:123], v[128:131], v[18:33]
	s_mov_b32 m0, s35
	s_waitcnt lgkmcnt(0)
	v_mfma_f32_32x32x16_f16 v[34:49], v[132:135], v[124:127], v[34:49]
	v_mfma_f32_32x32x16_f16 v[2:17], v[132:135], v[128:131], v[2:17]
	ds_read_b128 v[120:123], v96
	ds_read_b128 v[124:127], v113
	ds_read_b128 v[128:131], v113 offset:4096
	ds_read_b128 v[132:135], v112 offset:4096
	s_waitcnt lgkmcnt(2)
	v_mfma_f32_32x32x16_f16 v[50:65], v[120:123], v[124:127], v[50:65]
	s_waitcnt lgkmcnt(1)
	v_mfma_f32_32x32x16_f16 v[18:33], v[120:123], v[128:131], v[18:33]
	s_waitcnt lgkmcnt(0)
	v_mfma_f32_32x32x16_f16 v[34:49], v[132:135], v[124:127], v[34:49]
	v_mfma_f32_32x32x16_f16 v[2:17], v[132:135], v[128:131], v[2:17]
	ds_read_b128 v[120:123], v97
	ds_read_b128 v[124:127], v115
	ds_read_b128 v[128:131], v115 offset:4096
	ds_read_b128 v[132:135], v114 offset:4096
	buffer_load_dwordx4 v72, s[4:7], s43 offen lds
	s_mov_b32 m0, s36
	s_nop 0
	buffer_load_dwordx4 v74, s[4:7], s43 offen lds
	s_mov_b32 m0, s37
	s_waitcnt lgkmcnt(2)
	v_mfma_f32_32x32x16_f16 v[50:65], v[120:123], v[124:127], v[50:65]
	buffer_load_dwordx4 v73, s[12:15], s43 offen lds
	s_mov_b32 m0, s38
	s_nop 0
	buffer_load_dwordx4 v75, s[12:15], s43 offen lds
	s_waitcnt vmcnt(8)
	s_barrier
	s_add_i32 s43, s0, 0xb80
	s_waitcnt lgkmcnt(1)
	v_mfma_f32_32x32x16_f16 v[18:33], v[120:123], v[128:131], v[18:33]
	s_mov_b32 m0, s39
	s_waitcnt lgkmcnt(0)
	v_mfma_f32_32x32x16_f16 v[34:49], v[132:135], v[124:127], v[34:49]
	v_mfma_f32_32x32x16_f16 v[2:17], v[132:135], v[128:131], v[2:17]
	ds_read_b128 v[120:123], v98
	ds_read_b128 v[124:127], v117
	ds_read_b128 v[128:131], v117 offset:4096
	ds_read_b128 v[132:135], v116 offset:4096
	s_waitcnt lgkmcnt(2)
	v_mfma_f32_32x32x16_f16 v[50:65], v[120:123], v[124:127], v[50:65]
	s_waitcnt lgkmcnt(1)
	v_mfma_f32_32x32x16_f16 v[18:33], v[120:123], v[128:131], v[18:33]
	s_waitcnt lgkmcnt(0)
	v_mfma_f32_32x32x16_f16 v[34:49], v[132:135], v[124:127], v[34:49]
	v_mfma_f32_32x32x16_f16 v[2:17], v[132:135], v[128:131], v[2:17]
	ds_read_b128 v[120:123], v99
	ds_read_b128 v[124:127], v119
	ds_read_b128 v[128:131], v119 offset:4096
	ds_read_b128 v[132:135], v118 offset:4096
	buffer_load_dwordx4 v72, s[4:7], s43 offen lds
	s_mov_b32 m0, s40
	s_nop 0
	buffer_load_dwordx4 v74, s[4:7], s43 offen lds
	s_mov_b32 m0, s41
	s_waitcnt lgkmcnt(2)
	v_mfma_f32_32x32x16_f16 v[50:65], v[120:123], v[124:127], v[50:65]
	buffer_load_dwordx4 v73, s[12:15], s43 offen lds
	s_mov_b32 m0, s42
	s_nop 0
	buffer_load_dwordx4 v75, s[12:15], s43 offen lds
	s_waitcnt vmcnt(8)
	s_barrier
	s_add_i32 s43, s0, 0xc00
	s_waitcnt lgkmcnt(1)
	v_mfma_f32_32x32x16_f16 v[18:33], v[120:123], v[128:131], v[18:33]
	s_mov_b32 m0, s1
	s_waitcnt lgkmcnt(0)
	v_mfma_f32_32x32x16_f16 v[34:49], v[132:135], v[124:127], v[34:49]
	v_mfma_f32_32x32x16_f16 v[2:17], v[132:135], v[128:131], v[2:17]
	ds_read_b128 v[120:123], v110 offset:16384
	ds_read_b128 v[124:127], v111
	ds_read_b128 v[128:131], v111 offset:4096
	ds_read_b128 v[132:135], v110 offset:20480
	s_waitcnt lgkmcnt(2)
	v_mfma_f32_32x32x16_f16 v[50:65], v[120:123], v[124:127], v[50:65]
	s_waitcnt lgkmcnt(1)
	v_mfma_f32_32x32x16_f16 v[18:33], v[120:123], v[128:131], v[18:33]
	s_waitcnt lgkmcnt(0)
	v_mfma_f32_32x32x16_f16 v[34:49], v[132:135], v[124:127], v[34:49]
	v_mfma_f32_32x32x16_f16 v[2:17], v[132:135], v[128:131], v[2:17]
	ds_read_b128 v[120:123], v67 offset:16384
	ds_read_b128 v[124:127], v109
	ds_read_b128 v[128:131], v109 offset:4096
	ds_read_b128 v[132:135], v67 offset:20480
	buffer_load_dwordx4 v72, s[4:7], s43 offen lds
	s_mov_b32 m0, s2
	s_nop 0
	buffer_load_dwordx4 v74, s[4:7], s43 offen lds
	s_mov_b32 m0, s3
	s_waitcnt lgkmcnt(2)
	v_mfma_f32_32x32x16_f16 v[50:65], v[120:123], v[124:127], v[50:65]
	buffer_load_dwordx4 v73, s[12:15], s43 offen lds
	s_mov_b32 m0, s18
	s_nop 0
	buffer_load_dwordx4 v75, s[12:15], s43 offen lds
	s_waitcnt vmcnt(8)
	s_barrier
	s_add_i32 s43, s0, 0xc80
	s_waitcnt lgkmcnt(1)
	v_mfma_f32_32x32x16_f16 v[18:33], v[120:123], v[128:131], v[18:33]
	s_mov_b32 m0, s19
	s_add_i32 s19, s0, 0xd00
	s_waitcnt lgkmcnt(0)
	v_mfma_f32_32x32x16_f16 v[34:49], v[132:135], v[124:127], v[34:49]
	v_mfma_f32_32x32x16_f16 v[2:17], v[132:135], v[128:131], v[2:17]
	ds_read_b128 v[120:123], v110 offset:49152
	ds_read_b128 v[124:127], v111 offset:32768
	ds_read_b128 v[128:131], v111 offset:36864
	ds_read_b128 v[132:135], v110 offset:53248
	s_waitcnt lgkmcnt(2)
	v_mfma_f32_32x32x16_f16 v[50:65], v[120:123], v[124:127], v[50:65]
	s_waitcnt lgkmcnt(1)
	v_mfma_f32_32x32x16_f16 v[18:33], v[120:123], v[128:131], v[18:33]
	s_waitcnt lgkmcnt(0)
	v_mfma_f32_32x32x16_f16 v[34:49], v[132:135], v[124:127], v[34:49]
	v_mfma_f32_32x32x16_f16 v[2:17], v[132:135], v[128:131], v[2:17]
	ds_read_b128 v[120:123], v67 offset:49152
	ds_read_b128 v[124:127], v109 offset:32768
	ds_read_b128 v[128:131], v109 offset:36864
	ds_read_b128 v[132:135], v67 offset:53248
	buffer_load_dwordx4 v72, s[4:7], s43 offen lds
	s_mov_b32 m0, s31
	s_add_i32 s31, s0, 0xe00
	buffer_load_dwordx4 v74, s[4:7], s43 offen lds
	s_mov_b32 m0, s33
	s_waitcnt lgkmcnt(2)
	v_mfma_f32_32x32x16_f16 v[50:65], v[120:123], v[124:127], v[50:65]
	buffer_load_dwordx4 v73, s[12:15], s43 offen lds
	s_mov_b32 m0, s34
	s_nop 0
	buffer_load_dwordx4 v75, s[12:15], s43 offen lds
	s_waitcnt vmcnt(8)
	s_barrier
	s_mov_b32 m0, s35
	s_waitcnt lgkmcnt(1)
	v_mfma_f32_32x32x16_f16 v[18:33], v[120:123], v[128:131], v[18:33]
	s_waitcnt lgkmcnt(0)
	v_mfma_f32_32x32x16_f16 v[34:49], v[132:135], v[124:127], v[34:49]
	v_mfma_f32_32x32x16_f16 v[2:17], v[132:135], v[128:131], v[2:17]
	ds_read_b128 v[120:123], v96
	ds_read_b128 v[124:127], v113
	ds_read_b128 v[128:131], v113 offset:4096
	ds_read_b128 v[132:135], v112 offset:4096
	s_waitcnt lgkmcnt(2)
	v_mfma_f32_32x32x16_f16 v[50:65], v[120:123], v[124:127], v[50:65]
	s_waitcnt lgkmcnt(1)
	v_mfma_f32_32x32x16_f16 v[18:33], v[120:123], v[128:131], v[18:33]
	s_waitcnt lgkmcnt(0)
	v_mfma_f32_32x32x16_f16 v[34:49], v[132:135], v[124:127], v[34:49]
	v_mfma_f32_32x32x16_f16 v[2:17], v[132:135], v[128:131], v[2:17]
	ds_read_b128 v[120:123], v97
	ds_read_b128 v[124:127], v115
	ds_read_b128 v[128:131], v115 offset:4096
	ds_read_b128 v[132:135], v114 offset:4096
	buffer_load_dwordx4 v72, s[4:7], s19 offen lds
	s_mov_b32 m0, s36
	s_nop 0
	buffer_load_dwordx4 v74, s[4:7], s19 offen lds
	s_mov_b32 m0, s37
	s_waitcnt lgkmcnt(2)
	v_mfma_f32_32x32x16_f16 v[50:65], v[120:123], v[124:127], v[50:65]
	buffer_load_dwordx4 v73, s[12:15], s19 offen lds
	s_mov_b32 m0, s38
	s_nop 0
	buffer_load_dwordx4 v75, s[12:15], s19 offen lds
	s_waitcnt vmcnt(8)
	s_barrier
	s_add_i32 s19, s0, 0xd80
	s_waitcnt lgkmcnt(1)
	v_mfma_f32_32x32x16_f16 v[18:33], v[120:123], v[128:131], v[18:33]
	s_mov_b32 m0, s39
	s_ashr_i32 s0, s23, 31
	s_xor_b32 s0, s0, s25
	s_waitcnt lgkmcnt(0)
	v_mfma_f32_32x32x16_f16 v[34:49], v[132:135], v[124:127], v[34:49]
	v_mfma_f32_32x32x16_f16 v[2:17], v[132:135], v[128:131], v[2:17]
	ds_read_b128 v[120:123], v98
	ds_read_b128 v[124:127], v117
	ds_read_b128 v[128:131], v117 offset:4096
	ds_read_b128 v[132:135], v116 offset:4096
	s_waitcnt lgkmcnt(2)
	v_mfma_f32_32x32x16_f16 v[50:65], v[120:123], v[124:127], v[50:65]
	s_waitcnt lgkmcnt(1)
	v_mfma_f32_32x32x16_f16 v[18:33], v[120:123], v[128:131], v[18:33]
	s_waitcnt lgkmcnt(0)
	v_mfma_f32_32x32x16_f16 v[34:49], v[132:135], v[124:127], v[34:49]
	v_mfma_f32_32x32x16_f16 v[2:17], v[132:135], v[128:131], v[2:17]
	ds_read_b128 v[120:123], v99
	ds_read_b128 v[124:127], v119
	ds_read_b128 v[128:131], v119 offset:4096
	ds_read_b128 v[132:135], v118 offset:4096
	buffer_load_dwordx4 v72, s[4:7], s19 offen lds
	s_mov_b32 m0, s40
	s_nop 0
	buffer_load_dwordx4 v74, s[4:7], s19 offen lds
	s_mov_b32 m0, s41
	s_waitcnt lgkmcnt(2)
	v_mfma_f32_32x32x16_f16 v[50:65], v[120:123], v[124:127], v[50:65]
	buffer_load_dwordx4 v73, s[12:15], s19 offen lds
	s_mov_b32 m0, s42
	s_nop 0
	buffer_load_dwordx4 v75, s[12:15], s19 offen lds
	s_waitcnt vmcnt(8)
	s_barrier
	s_mov_b32 m0, s1
	s_waitcnt lgkmcnt(1)
	v_mfma_f32_32x32x16_f16 v[18:33], v[120:123], v[128:131], v[18:33]
	s_abs_i32 s1, s23
	s_waitcnt lgkmcnt(0)
	v_mfma_f32_32x32x16_f16 v[34:49], v[132:135], v[124:127], v[34:49]
	v_mfma_f32_32x32x16_f16 v[2:17], v[132:135], v[128:131], v[2:17]
	ds_read_b128 v[120:123], v110 offset:16384
	ds_read_b128 v[124:127], v111
	ds_read_b128 v[128:131], v111 offset:4096
	ds_read_b128 v[132:135], v110 offset:20480
	s_waitcnt lgkmcnt(2)
	v_mfma_f32_32x32x16_f16 v[50:65], v[120:123], v[124:127], v[50:65]
	s_waitcnt lgkmcnt(1)
	v_mfma_f32_32x32x16_f16 v[18:33], v[120:123], v[128:131], v[18:33]
	s_waitcnt lgkmcnt(0)
	v_mfma_f32_32x32x16_f16 v[34:49], v[132:135], v[124:127], v[34:49]
	v_mfma_f32_32x32x16_f16 v[2:17], v[132:135], v[128:131], v[2:17]
	ds_read_b128 v[120:123], v67 offset:16384
	ds_read_b128 v[124:127], v109
	ds_read_b128 v[128:131], v109 offset:4096
	ds_read_b128 v[132:135], v67 offset:20480
	buffer_load_dwordx4 v72, s[4:7], s31 offen lds
	s_mov_b32 m0, s2
	s_mul_hi_u32 s2, s1, s26
	buffer_load_dwordx4 v74, s[4:7], s31 offen lds
	s_mov_b32 m0, s3
	s_mul_i32 s3, s2, s24
	s_waitcnt lgkmcnt(2)
	v_mfma_f32_32x32x16_f16 v[50:65], v[120:123], v[124:127], v[50:65]
	buffer_load_dwordx4 v73, s[12:15], s31 offen lds
	s_mov_b32 m0, s18
	s_sub_i32 s1, s1, s3
	buffer_load_dwordx4 v75, s[12:15], s31 offen lds
	s_waitcnt vmcnt(8)
	s_barrier
	s_add_i32 s3, s2, 1
	s_waitcnt lgkmcnt(1)
	v_mfma_f32_32x32x16_f16 v[18:33], v[120:123], v[128:131], v[18:33]
	s_sub_i32 s14, s1, s24
	s_cmp_ge_u32 s1, s24
	s_cselect_b32 s2, s3, s2
	s_cselect_b32 s1, s14, s1
	s_add_i32 s3, s2, 1
	s_cmp_ge_u32 s1, s24
	s_cselect_b32 s1, s3, s2
	s_waitcnt lgkmcnt(0)
	v_mfma_f32_32x32x16_f16 v[34:49], v[132:135], v[124:127], v[34:49]
	s_xor_b32 s1, s1, s0
	s_sub_i32 s0, s1, s0
	s_mul_i32 s1, s0, s21
	s_sub_i32 s15, s23, s1
	s_lshl_b32 s2, s15, 7
	s_lshl_b32 s14, s0, 7
	s_ashr_i32 s3, s2, 31
	v_mfma_f32_32x32x16_f16 v[2:17], v[132:135], v[128:131], v[2:17]
	ds_read_b128 v[120:123], v110 offset:49152
	ds_read_b128 v[124:127], v111 offset:32768
	ds_read_b128 v[128:131], v111 offset:36864
	ds_read_b128 v[132:135], v110 offset:53248
	s_waitcnt lgkmcnt(2)
	v_mfma_f32_32x32x16_f16 v[50:65], v[120:123], v[124:127], v[50:65]
	s_waitcnt lgkmcnt(1)
	v_mfma_f32_32x32x16_f16 v[18:33], v[120:123], v[128:131], v[18:33]
	s_waitcnt lgkmcnt(0)
	v_mfma_f32_32x32x16_f16 v[34:49], v[132:135], v[124:127], v[34:49]
	v_mfma_f32_32x32x16_f16 v[2:17], v[132:135], v[128:131], v[2:17]
	ds_read_b128 v[120:123], v67 offset:49152
	ds_read_b128 v[124:127], v109 offset:32768
	ds_read_b128 v[128:131], v109 offset:36864
	ds_read_b128 v[132:135], v67 offset:53248
	s_waitcnt vmcnt(4)
	s_barrier
	s_waitcnt lgkmcnt(2)
	v_mfma_f32_32x32x16_f16 v[50:65], v[120:123], v[124:127], v[50:65]
	s_waitcnt lgkmcnt(1)
	v_mfma_f32_32x32x16_f16 v[18:33], v[120:123], v[128:131], v[18:33]
	s_waitcnt lgkmcnt(0)
	v_mfma_f32_32x32x16_f16 v[34:49], v[132:135], v[124:127], v[34:49]
	v_mfma_f32_32x32x16_f16 v[2:17], v[132:135], v[128:131], v[2:17]
	ds_read_b128 v[120:123], v96
	ds_read_b128 v[124:127], v113
	ds_read_b128 v[128:131], v113 offset:4096
	ds_read_b128 v[110:113], v112 offset:4096
	s_waitcnt lgkmcnt(2)
	v_mfma_f32_32x32x16_f16 v[50:65], v[120:123], v[124:127], v[50:65]
	s_waitcnt lgkmcnt(1)
	v_mfma_f32_32x32x16_f16 v[18:33], v[120:123], v[128:131], v[18:33]
	s_waitcnt lgkmcnt(0)
	v_mfma_f32_32x32x16_f16 v[34:49], v[110:113], v[124:127], v[34:49]
	ds_read_b128 v[120:123], v97
	ds_read_b128 v[124:127], v115
	ds_read_b128 v[132:135], v115 offset:4096
	s_waitcnt lgkmcnt(1)
	v_mfma_f32_32x32x16_f16 v[50:65], v[120:123], v[124:127], v[50:65]
	s_waitcnt lgkmcnt(0)
	v_mfma_f32_32x32x16_f16 v[18:33], v[120:123], v[132:135], v[18:33]
	ds_read_b128 v[120:123], v114 offset:4096
	s_waitcnt vmcnt(0)
	s_barrier
	v_mfma_f32_32x32x16_f16 v[2:17], v[110:113], v[128:131], v[2:17]
	s_waitcnt lgkmcnt(0)
	v_mfma_f32_32x32x16_f16 v[34:49], v[120:123], v[124:127], v[34:49]
	ds_read_b128 v[124:127], v98
	ds_read_b128 v[136:139], v117
	ds_read_b128 v[140:143], v117 offset:4096
	ds_read_b128 v[114:117], v116 offset:4096
	s_waitcnt lgkmcnt(2)
	v_mfma_f32_32x32x16_f16 v[50:65], v[124:127], v[136:139], v[50:65]
	s_waitcnt lgkmcnt(1)
	v_mfma_f32_32x32x16_f16 v[18:33], v[124:127], v[140:143], v[18:33]
	v_mfma_f32_32x32x16_f16 v[2:17], v[120:123], v[132:135], v[2:17]
	s_waitcnt lgkmcnt(0)
	v_mfma_f32_32x32x16_f16 v[34:49], v[114:117], v[136:139], v[34:49]
	ds_read_b128 v[124:127], v99
	ds_read_b128 v[136:139], v119
	ds_read_b128 v[144:147], v119 offset:4096
	s_waitcnt lgkmcnt(1)
	v_mfma_f32_32x32x16_f16 v[50:65], v[124:127], v[136:139], v[50:65]
	s_waitcnt lgkmcnt(0)
	v_mfma_f32_32x32x16_f16 v[18:33], v[124:127], v[144:147], v[18:33]
	ds_read_b128 v[124:127], v118 offset:4096
	s_waitcnt lgkmcnt(0)
	s_barrier
	s_nop 8
	ds_write_b128 v100, v[50:53]
	ds_write_b128 v101, v[54:57]
	v_mfma_f32_32x32x16_f16 v[2:17], v[114:117], v[140:143], v[2:17]
	s_waitcnt lgkmcnt(2)
	v_mfma_f32_32x32x16_f16 v[2:17], v[124:127], v[144:147], v[2:17]
	v_mfma_f32_32x32x16_f16 v[34:49], v[124:127], v[136:139], v[34:49]
	ds_write_b128 v102, v[58:61]
	ds_write_b128 v103, v[62:65]
	s_nop 9
	ds_write_b128 v104, v[34:37]
	ds_write_b128 v105, v[38:41]
	ds_write_b128 v106, v[42:45]
	ds_write_b128 v107, v[46:49]
	ds_write_b128 v100, v[18:21] offset:16384
	ds_write_b128 v101, v[22:25] offset:16384
	ds_write_b128 v102, v[26:29] offset:16384
	ds_write_b128 v103, v[30:33] offset:16384
	ds_write_b128 v104, v[2:5] offset:16384
	ds_write_b128 v105, v[6:9] offset:16384
	ds_write_b128 v106, v[10:13] offset:16384
	ds_write_b128 v107, v[14:17] offset:16384
	v_or_b32_e32 v25, s14, v1
	s_waitcnt lgkmcnt(0)
	s_barrier
	v_mov_b64_e32 v[10:11], v[160:161]
	v_mov_b64_e32 v[12:13], v[162:163]
	v_mov_b64_e32 v[6:7], v[176:177]
	v_mov_b64_e32 v[8:9], v[178:179]
	v_mov_b64_e32 v[2:3], v[180:181]
	v_mov_b64_e32 v[4:5], v[182:183]
	v_add_u32_e32 v14, 0, v85
	v_add_u32_e32 v18, s28, v85
	ds_read_b128 v[14:17], v14
	ds_read_b128 v[26:29], v18
	v_mov_b64_e32 v[18:19], v[164:165]
	v_mov_b64_e32 v[20:21], v[166:167]
	s_waitcnt lgkmcnt(0)
	v_pk_add_f32 v[16:17], v[16:17], v[28:29]
	v_add_f32_e32 v35, v14, v26
	v_mov_b32_e32 v34, v27
	v_cvt_f32_f16_e32 v30, v11
	v_cvt_f32_f16_sdwa v31, v11 dst_sel:DWORD dst_unused:UNUSED_PAD src0_sel:WORD_1
	v_add_u32_e32 v11, 0, v86
	v_pk_add_f32 v[16:17], v[8:9], v[16:17]
	ds_read_b128 v[26:29], v11
	v_add_u32_e32 v11, s28, v86
	v_pk_add_f32 v[36:37], v[16:17], v[30:31]
	ds_read_b128 v[30:33], v11
	v_cvt_f32_f16_e32 v38, v13
	v_cvt_f32_f16_sdwa v39, v13 dst_sel:DWORD dst_unused:UNUSED_PAD src0_sel:WORD_1
	v_mov_b32_e32 v16, v2
	v_mov_b32_e32 v17, v3
	s_waitcnt lgkmcnt(0)
	v_pk_add_f32 v[28:29], v[28:29], v[32:33]
	v_cvt_f32_f16_e32 v32, v10
	v_pk_add_f32 v[28:29], v[4:5], v[28:29]
	v_pk_mov_b32 v[16:17], v[26:27], v[16:17] op_sel:[1,0]
	v_pk_add_f32 v[28:29], v[28:29], v[38:39]
	v_cvt_f32_f16_e32 v38, v12
	v_add_f32_e32 v26, v26, v30
	v_cvt_f32_f16_sdwa v33, v10 dst_sel:DWORD dst_unused:UNUSED_PAD src0_sel:WORD_1
	v_cvt_f32_f16_sdwa v30, v12 dst_sel:DWORD dst_unused:UNUSED_PAD src0_sel:WORD_1
	v_pk_mov_b32 v[14:15], v[14:15], v[6:7] op_sel:[1,0]
	v_mov_b32_e32 v10, v31
	v_mov_b32_e32 v11, v26
	v_pk_add_f32 v[44:45], v[14:15], v[34:35]
	v_mov_b32_e32 v12, v7
	v_mov_b32_e32 v13, v32
	v_pk_add_f32 v[10:11], v[16:17], v[10:11]
	v_pk_add_f32 v[46:47], v[12:13], v[44:45]
	v_mov_b32_e32 v22, v3
	v_mov_b32_e32 v23, v38
	v_pk_add_f32 v[48:49], v[22:23], v[10:11]
	v_mov_b32_e32 v10, v33
	v_mov_b32_e32 v11, v47
	v_pk_add_f32 v[50:51], v[46:47], v[10:11]
	v_mov_b64_e32 v[14:15], v[168:169]
	v_mov_b64_e32 v[16:17], v[170:171]
	v_mov_b64_e32 v[10:11], v[172:173]
	v_mov_b64_e32 v[12:13], v[174:175]
	v_mov_b32_e32 v31, v49
	v_pk_add_f32 v[40:41], v[48:49], v[30:31]
	v_pk_mov_b32 v[30:31], v[34:35], v[44:45] op_sel:[1,0]
	v_mov_b32_e32 v27, v44
	v_mov_b32_e32 v3, v7
	v_pk_add_f32 v[30:31], v[6:7], v[30:31]
	v_mov_b32_e32 v39, v33
	v_pk_add_f32 v[26:27], v[2:3], v[26:27]
	v_pk_add_f32 v[30:31], v[30:31], v[32:33]
	v_pk_add_f32 v[26:27], v[26:27], v[38:39]
	v_pk_mul_f32 v[32:33], v[46:47], v[46:47]
	v_pk_add_f32 v[34:35], v[30:31], v[26:27]
	v_pk_mul_f32 v[26:27], v[30:31], v[26:27]
	v_mov_b32_e32 v51, v33
	v_pk_mul_f32 v[32:33], v[48:49], v[48:49]
	v_mov_b32_e32 v35, v27
	v_pk_mul_f32 v[26:27], v[40:41], v[40:41]
	v_mov_b32_e32 v32, v40
	v_mov_b32_e32 v67, v26
	v_pk_add_f32 v[32:33], v[50:51], v[32:33]
	v_pk_add_f32 v[26:27], v[34:35], v[66:67]
	v_pk_mul_f32 v[30:31], v[36:37], v[36:37]
	v_pk_mul_f32 v[34:35], v[28:29], v[28:29]
	v_pk_add_f32 v[26:27], v[32:33], v[26:27]
	v_mov_b32_e32 v32, v36
	v_mov_b32_e32 v33, v30
	v_mov_b32_e32 v38, v28
	v_mov_b32_e32 v39, v34
	v_pk_add_f32 v[32:33], v[32:33], v[38:39]
	v_mov_b32_e32 v30, v37
	v_mov_b32_e32 v34, v29
	v_pk_add_f32 v[26:27], v[26:27], v[32:33]
	v_pk_add_f32 v[30:31], v[30:31], v[34:35]
	v_pk_add_f32 v[26:27], v[26:27], v[30:31]
	s_nop 1
	v_mov_b32_dpp v32, v26 row_mirror row_mask:0xf bank_mask:0xf
	v_mov_b32_dpp v33, v27 row_mirror row_mask:0xf bank_mask:0xf
	v_cvt_pk_f16_f32 v39, v28, v29
	v_cvt_pk_f16_f32 v37, v36, v37
	s_waitcnt lgkmcnt(0)
	v_pk_add_f32 v[26:27], v[26:27], v[32:33]
	s_nop 1
	v_mov_b32_dpp v32, v26 row_half_mirror row_mask:0xf bank_mask:0xf
	v_mov_b32_dpp v33, v27 row_half_mirror row_mask:0xf bank_mask:0xf
	v_cvt_pk_f16_f32 v36, v47, v50
	v_cvt_pk_f16_f32 v38, v49, v40
	s_waitcnt lgkmcnt(0)
	v_pk_add_f32 v[26:27], v[26:27], v[32:33]
	s_nop 1
	v_mov_b32_dpp v28, v26 quad_perm:[2,3,0,1] row_mask:0xf bank_mask:0xf
	v_mov_b32_dpp v29, v27 quad_perm:[2,3,0,1] row_mask:0xf bank_mask:0xf
	v_or_b32_e32 v32, s2, v78
	v_mul_lo_u32 v24, v25, s30
	v_add_lshl_u32 v24, v32, v24, 1
	buffer_store_dwordx4 v[36:39], v24, s[8:11], 0 offen sc1
	s_waitcnt lgkmcnt(0)
	v_pk_add_f32 v[26:27], v[26:27], v[28:29]
	s_lshl_b32 s2, s15, 4
	v_mov_b32_e32 v24, v7
	s_nop 1
	v_mov_b32_dpp v28, v26 quad_perm:[1,0,3,2] row_mask:0xf bank_mask:0xf
	v_mov_b32_dpp v29, v27 quad_perm:[1,0,3,2] row_mask:0xf bank_mask:0xf
	s_and_saveexec_b64 s[0:1], vcc
	s_cbranch_execz .LBB9_5
	s_waitcnt lgkmcnt(0)
	v_pk_add_f32 v[64:65], v[26:27], v[28:29]
	v_lshl_add_u32 v23, v25, 6, s2
	v_mov_b32_e32 v67, v66
	s_mov_b32 s18, s10
	s_mov_b32 s19, s11
	buffer_store_dwordx4 v[64:67], v23, s[16:19], 0 offen sc1
